# speedup vs baseline: 1.0004x; 1.0004x over previous
.LBB4_3:
	s_lshr_b32 s29, s35, 25
	s_add_i32 s29, s34, s29
	s_not_b32 s62, s30
	s_ashr_i32 s63, s29, 7
	s_add_i32 s64, s54, 0x18000
	v_and_b32_e32 v19, 15, v0
	v_and_b32_e32 v0, 4, v0
	s_add_u32 s30, s38, 0x80
	v_lshl_or_b32 v149, s15, 6, v19
	v_lshlrev_b32_e32 v20, 5, v1
	v_and_or_b32 v0, v18, 1, v0
	s_waitcnt vmcnt(0)
	s_barrier
	s_addc_u32 s31, s39, 0
	s_mov_b32 m0, s64
	s_nop 0
	global_load_lds_dwordx4 v148, s[30:31]
	s_add_i32 s65, s54, 0x1a000
	s_add_i32 s66, s54, 0x8000
	v_lshlrev_b32_e32 v21, 7, v149
	v_lshlrev_b32_e32 v0, 4, v0
	v_or_b32_e32 v23, 16, v20
	s_mov_b32 m0, s65
	s_nop 0
	global_load_lds_dwordx4 v152, s[30:31]
	s_add_u32 s30, s40, 0x80
	v_xor_b32_e32 v18, v0, v20
	v_bitop3_b32 v22, v21, v0, v20 bitop3:0xf6
	v_bitop3_b32 v20, v0, v20, 16 bitop3:0x1e
	v_bitop3_b32 v21, v21, v0, v23 bitop3:0xf6
	v_lshlrev_b32_e32 v0, 7, v19
	s_addc_u32 s31, s41, 0
	s_mov_b32 m0, s66
	s_nop 0
	global_load_lds_dwordx4 v146, s[30:31]
	s_add_i32 s67, s54, 0xa000
	s_add_i32 s68, s54, 0x1c000
	v_lshl_or_b32 v0, s4, 12, v0
	s_mov_b32 m0, s67
	s_nop 0
	global_load_lds_dwordx4 v150, s[30:31]
	s_add_u32 s0, s0, 0x80
	v_or3_b32 v18, v18, v0, s5
	v_or3_b32 v19, v20, v0, s5
	s_addc_u32 s1, s1, 0
	s_mov_b32 m0, s68
	s_nop 0
	global_load_lds_dwordx4 v148, s[0:1]
	v_lshlrev_b32_e32 v0, 4, v1
	s_add_i32 s69, s54, 0x1e000
	s_mov_b32 m0, s69
	s_nop 0
	global_load_lds_dwordx4 v152, s[0:1]
	v_and_b32_e32 v1, 32, v0
	v_and_b32_e32 v153, 16, v0
	v_or_b32_e32 v158, 32, v0
	v_div_scale_f32 v0, s[0:1], s13, s13, 1.0
	v_lshl_or_b32 v151, s4, 6, v1
	v_rcp_f32_e32 v1, v0
	s_cmpk_gt_i32 s34, 0x7f
	s_cselect_b64 s[30:31], -1, 0
	s_add_i32 s70, s54, 0xc000
	v_fma_f32 v20, -v0, v1, 1.0
	v_fmac_f32_e32 v1, v20, v1
	v_div_scale_f32 v20, vcc, 1.0, s13, 1.0
	v_mul_f32_e32 v23, v20, v1
	v_fma_f32 v24, -v0, v23, v20
	v_fmac_f32_e32 v23, v24, v1
	v_fma_f32 v0, -v0, v23, v20
	v_div_fmas_f32 v0, v0, v1, v23
	v_mov_b32_e32 v1, s14
	v_mul_f32_e32 v1, s13, v1
	v_div_scale_f32 v20, s[0:1], v1, v1, 1.0
	v_rcp_f32_e32 v23, v20
	s_add_i32 s71, s54, 0xe000
	s_ashr_i32 s72, s33, 31
	s_ashr_i32 s73, s2, 31
	v_fma_f32 v24, -v20, v23, 1.0
	v_fmac_f32_e32 v23, v24, v23
	v_div_scale_f32 v24, vcc, 1.0, v1, 1.0
	v_mul_f32_e32 v25, v24, v23
	v_fma_f32 v26, -v20, v25, v24
	v_fmac_f32_e32 v25, v26, v23
	v_fma_f32 v20, -v20, v25, v24
	s_waitcnt vmcnt(6)
	global_load_dword v245, v147, s[10:11]
	global_load_dword v245, v147, s[10:11]
	global_load_dword v245, v147, s[10:11]
	global_load_dword v245, v147, s[10:11]
	v_div_fmas_f32 v20, v20, v23, v25
	s_cmp_eq_u32 s63, 2
	v_div_fixup_f32 v0, v0, s13, 1.0
	v_div_fixup_f32 v159, v20, v1, 1.0
	s_cselect_b64 s[14:15], -1, 0
	s_cmpk_gt_u32 s34, 0x17f
	v_mov_b32_e32 v154, v0
	v_mov_b32_e32 v155, v0
	v_mul_f32_e32 v160, 0x40c00000, v159
	s_cselect_b64 s[34:35], -1, 0
	v_add_u32_e32 v161, 0, v18
	v_add_u32_e32 v162, 0, v19
	v_add_u32_e32 v163, 0, v22
	v_add_u32_e32 v164, 0, v21
	s_barrier
	s_branch .LBB4_5

.Lrs_a_4:
	s_add_u32 s81, s40, s22
	s_addc_u32 s82, s41, s23
	s_add_u32 s29, s40, 0x100
	s_addc_u32 s44, s41, 0
	s_and_b64 s[42:43], s[14:15], exec
	ds_read_b128 v[82:85], v161
	ds_read_b128 v[94:97], v161 offset:2048
	ds_read_b128 v[102:105], v162
	ds_read_b128 v[110:113], v162 offset:2048
	s_cselect_b32 s47, s37, s44
	s_cselect_b32 s46, s36, s29
	s_add_u32 s29, s38, 0x100
	s_addc_u32 s44, s39, 0
	s_and_b64 s[42:43], s[14:15], exec
	s_cselect_b32 s49, s5, s44
	s_cselect_b32 s48, s4, s29
	s_add_u32 s44, s46, 0x80
	s_addc_u32 s45, s47, 0
	s_add_u32 s42, s48, 0x80
	s_addc_u32 s43, s49, 0
	ds_read_b128 v[58:61], v163
	ds_read_b128 v[66:69], v163 offset:2048
	ds_read_b128 v[62:65], v164
	ds_read_b128 v[70:73], v164 offset:2048
	ds_read_b128 v[74:77], v163 offset:4096
	ds_read_b128 v[86:89], v163 offset:6144
	ds_read_b128 v[78:81], v164 offset:4096
	ds_read_b128 v[90:93], v164 offset:6144
	s_add_u32 s78, s81, 0x80
	s_addc_u32 s79, s82, 0
	s_mov_b32 m0, s70
	s_nop 0
	global_load_lds_dwordx4 v146, s[78:79]
	s_mov_b32 m0, s71
	s_nop 0
	global_load_lds_dwordx4 v150, s[78:79]
	s_waitcnt lgkmcnt(8)
	ds_read_b128 v[142:145], v161 offset:16384
	ds_read_b128 v[166:169], v161 offset:18432
	ds_read_b128 v[170:173], v162 offset:16384
	ds_read_b128 v[174:177], v162 offset:18432
	s_waitcnt vmcnt(12)
	s_waitcnt lgkmcnt(0)
	s_barrier
	s_waitcnt lgkmcnt(0)
	s_waitcnt vmcnt(16)
	v_mov_b32_e32 v1, v0
	v_pk_mul_f32 v[16:17], v[0:1], v[16:17]
	v_pk_mul_f32 v[14:15], v[154:155], v[14:15]
	v_pk_mul_f32 v[12:13], v[0:1], v[12:13]
	v_pk_mul_f32 v[10:11], v[154:155], v[10:11]
	v_pk_mul_f32 v[8:9], v[0:1], v[8:9]
	v_pk_mul_f32 v[6:7], v[154:155], v[6:7]
	v_pk_mul_f32 v[4:5], v[0:1], v[4:5]
	v_pk_mul_f32 v[2:3], v[154:155], v[2:3]
	s_setprio 1
	v_mfma_f32_16x16x128_f8f6f4 v[18:21], v[82:85], v[58:61], v[14:17] cbsz:4 blgp:4
	v_mfma_f32_16x16x128_f8f6f4 v[18:21], v[102:105], v[62:65], v[18:21] cbsz:4 blgp:4
	v_mfma_f32_16x16x128_f8f6f4 v[22:25], v[94:97], v[58:61], v[10:13] cbsz:4 blgp:4
	v_mfma_f32_16x16x128_f8f6f4 v[22:25], v[110:113], v[62:65], v[22:25] cbsz:4 blgp:4
	v_mfma_f32_16x16x128_f8f6f4 v[50:53], v[142:145], v[58:61], v[6:9] cbsz:4 blgp:4
	v_mfma_f32_16x16x128_f8f6f4 v[50:53], v[170:173], v[62:65], v[50:53] cbsz:4 blgp:4
	v_mfma_f32_16x16x128_f8f6f4 v[54:57], v[166:169], v[58:61], v[2:5] cbsz:4 blgp:4
	v_mfma_f32_16x16x128_f8f6f4 v[54:57], v[174:177], v[62:65], v[54:57] cbsz:4 blgp:4
	v_mfma_f32_16x16x128_f8f6f4 v[26:29], v[82:85], v[66:69], v[14:17] cbsz:4 blgp:4
	v_mfma_f32_16x16x128_f8f6f4 v[26:29], v[102:105], v[70:73], v[26:29] cbsz:4 blgp:4
	v_mfma_f32_16x16x128_f8f6f4 v[30:33], v[94:97], v[66:69], v[10:13] cbsz:4 blgp:4
	v_mfma_f32_16x16x128_f8f6f4 v[30:33], v[110:113], v[70:73], v[30:33] cbsz:4 blgp:4
	v_mfma_f32_16x16x128_f8f6f4 v[58:61], v[142:145], v[66:69], v[6:9] cbsz:4 blgp:4
	v_mfma_f32_16x16x128_f8f6f4 v[58:61], v[170:173], v[70:73], v[58:61] cbsz:4 blgp:4
	v_mfma_f32_16x16x128_f8f6f4 v[62:65], v[166:169], v[66:69], v[2:5] cbsz:4 blgp:4
	v_mfma_f32_16x16x128_f8f6f4 v[62:65], v[174:177], v[70:73], v[62:65] cbsz:4 blgp:4
	v_mfma_f32_16x16x128_f8f6f4 v[34:37], v[82:85], v[74:77], v[14:17] cbsz:4 blgp:4
	v_mfma_f32_16x16x128_f8f6f4 v[34:37], v[102:105], v[78:81], v[34:37] cbsz:4 blgp:4
	v_mfma_f32_16x16x128_f8f6f4 v[38:41], v[94:97], v[74:77], v[10:13] cbsz:4 blgp:4
	v_mfma_f32_16x16x128_f8f6f4 v[38:41], v[110:113], v[78:81], v[38:41] cbsz:4 blgp:4
	v_mfma_f32_16x16x128_f8f6f4 v[66:69], v[142:145], v[74:77], v[6:9] cbsz:4 blgp:4
	v_mfma_f32_16x16x128_f8f6f4 v[66:69], v[170:173], v[78:81], v[66:69] cbsz:4 blgp:4
	v_mfma_f32_16x16x128_f8f6f4 v[70:73], v[166:169], v[74:77], v[2:5] cbsz:4 blgp:4
	v_mfma_f32_16x16x128_f8f6f4 v[70:73], v[174:177], v[78:81], v[70:73] cbsz:4 blgp:4
	v_mfma_f32_16x16x128_f8f6f4 v[42:45], v[82:85], v[86:89], v[14:17] cbsz:4 blgp:4
	v_mfma_f32_16x16x128_f8f6f4 v[42:45], v[102:105], v[90:93], v[42:45] cbsz:4 blgp:4
	v_mfma_f32_16x16x128_f8f6f4 v[46:49], v[94:97], v[86:89], v[10:13] cbsz:4 blgp:4
	v_mfma_f32_16x16x128_f8f6f4 v[46:49], v[110:113], v[90:93], v[46:49] cbsz:4 blgp:4
	v_mfma_f32_16x16x128_f8f6f4 v[74:77], v[142:145], v[86:89], v[6:9] cbsz:4 blgp:4
	v_mfma_f32_16x16x128_f8f6f4 v[74:77], v[170:173], v[90:93], v[74:77] cbsz:4 blgp:4
	v_mfma_f32_16x16x128_f8f6f4 v[78:81], v[166:169], v[86:89], v[2:5] cbsz:4 blgp:4
	v_mfma_f32_16x16x128_f8f6f4 v[78:81], v[174:177], v[90:93], v[78:81] cbsz:4 blgp:4
	s_setprio 0
	s_barrier
	s_mov_b32 m0, s55
	s_nop 0
	global_load_lds_dwordx4 v148, s[48:49]
	s_mov_b32 m0, s56
	s_nop 0
	global_load_lds_dwordx4 v152, s[48:49]
	ds_read_b128 v[114:117], v163 offset:16384
	ds_read_b128 v[122:125], v163 offset:18432
	ds_read_b128 v[130:133], v164 offset:16384
	ds_read_b128 v[134:137], v164 offset:18432
	ds_read_b128 v[178:181], v163 offset:20480
	ds_read_b128 v[182:185], v163 offset:22528
	ds_read_b128 v[186:189], v164 offset:20480
	ds_read_b128 v[190:193], v164 offset:22528
	s_mov_b32 m0, s54
	s_nop 0
	global_load_lds_dwordx4 v146, s[46:47]
	s_mov_b32 m0, s57
	s_nop 0
	global_load_lds_dwordx4 v150, s[46:47]
	s_add_u32 s48, s48, s24
	s_addc_u32 s49, s49, s25
	s_mov_b32 m0, s58
	s_nop 0
	global_load_lds_dwordx4 v148, s[48:49]
	s_mov_b32 m0, s59
	s_nop 0
	global_load_lds_dwordx4 v152, s[48:49]
	s_waitcnt vmcnt(12)
	s_waitcnt lgkmcnt(0)
	s_barrier
	s_setprio 1
	v_mfma_f32_16x16x128_f8f6f4 v[86:89], v[82:85], v[114:117], v[14:17] cbsz:4 blgp:4
	v_mfma_f32_16x16x128_f8f6f4 v[86:89], v[102:105], v[130:133], v[86:89] cbsz:4 blgp:4
	v_mfma_f32_16x16x128_f8f6f4 v[90:93], v[94:97], v[114:117], v[10:13] cbsz:4 blgp:4
	v_mfma_f32_16x16x128_f8f6f4 v[90:93], v[110:113], v[130:133], v[90:93] cbsz:4 blgp:4
	v_mfma_f32_16x16x128_f8f6f4 v[98:101], v[82:85], v[122:125], v[14:17] cbsz:4 blgp:4
	v_mfma_f32_16x16x128_f8f6f4 v[98:101], v[102:105], v[134:137], v[98:101] cbsz:4 blgp:4
	v_mfma_f32_16x16x128_f8f6f4 v[106:109], v[94:97], v[122:125], v[10:13] cbsz:4 blgp:4
	v_mfma_f32_16x16x128_f8f6f4 v[106:109], v[110:113], v[134:137], v[106:109] cbsz:4 blgp:4
	v_mfma_f32_16x16x128_f8f6f4 v[118:121], v[82:85], v[178:181], v[14:17] cbsz:4 blgp:4
	v_mfma_f32_16x16x128_f8f6f4 v[118:121], v[102:105], v[186:189], v[118:121] cbsz:4 blgp:4
	v_mfma_f32_16x16x128_f8f6f4 v[126:129], v[94:97], v[178:181], v[10:13] cbsz:4 blgp:4
	v_mfma_f32_16x16x128_f8f6f4 v[126:129], v[110:113], v[186:189], v[126:129] cbsz:4 blgp:4
	v_mfma_f32_16x16x128_f8f6f4 v[138:141], v[82:85], v[182:185], v[14:17] cbsz:4 blgp:4
	v_mfma_f32_16x16x128_f8f6f4 v[138:141], v[102:105], v[190:193], v[138:141] cbsz:4 blgp:4
	v_mfma_f32_16x16x128_f8f6f4 v[82:85], v[94:97], v[182:185], v[10:13] cbsz:4 blgp:4
	v_mfma_f32_16x16x128_f8f6f4 v[82:85], v[110:113], v[190:193], v[82:85] cbsz:4 blgp:4
	v_mfma_f32_16x16x128_f8f6f4 v[94:97], v[142:145], v[114:117], v[6:9] cbsz:4 blgp:4
	v_mfma_f32_16x16x128_f8f6f4 v[94:97], v[170:173], v[130:133], v[94:97] cbsz:4 blgp:4
	v_mfma_f32_16x16x128_f8f6f4 v[102:105], v[166:169], v[114:117], v[2:5] cbsz:4 blgp:4
	v_mfma_f32_16x16x128_f8f6f4 v[102:105], v[174:177], v[130:133], v[102:105] cbsz:4 blgp:4
	v_mfma_f32_16x16x128_f8f6f4 v[110:113], v[142:145], v[122:125], v[6:9] cbsz:4 blgp:4
	v_mfma_f32_16x16x128_f8f6f4 v[110:113], v[170:173], v[134:137], v[110:113] cbsz:4 blgp:4
	v_mfma_f32_16x16x128_f8f6f4 v[114:117], v[166:169], v[122:125], v[2:5] cbsz:4 blgp:4
	v_mfma_f32_16x16x128_f8f6f4 v[114:117], v[174:177], v[134:137], v[114:117] cbsz:4 blgp:4
	v_mfma_f32_16x16x128_f8f6f4 v[122:125], v[142:145], v[178:181], v[6:9] cbsz:4 blgp:4
	v_mfma_f32_16x16x128_f8f6f4 v[122:125], v[170:173], v[186:189], v[122:125] cbsz:4 blgp:4
	v_mfma_f32_16x16x128_f8f6f4 v[130:133], v[166:169], v[178:181], v[2:5] cbsz:4 blgp:4
	v_mfma_f32_16x16x128_f8f6f4 v[130:133], v[174:177], v[186:189], v[130:133] cbsz:4 blgp:4
	v_mfma_f32_16x16x128_f8f6f4 v[134:137], v[142:145], v[182:185], v[6:9] cbsz:4 blgp:4
	v_mfma_f32_16x16x128_f8f6f4 v[134:137], v[170:173], v[190:193], v[134:137] cbsz:4 blgp:4
	v_mfma_f32_16x16x128_f8f6f4 v[142:145], v[166:169], v[182:185], v[2:5] cbsz:4 blgp:4
	v_mfma_f32_16x16x128_f8f6f4 v[142:145], v[174:177], v[190:193], v[142:145] cbsz:4 blgp:4
	s_setprio 0
	s_barrier
	ds_read_b128 v[166:169], v161 offset:32768
	ds_read_b128 v[170:173], v161 offset:34816
	ds_read_b128 v[174:177], v162 offset:32768
	ds_read_b128 v[178:181], v162 offset:34816
	ds_read_b128 v[182:185], v163 offset:32768
	ds_read_b128 v[186:189], v163 offset:34816
	ds_read_b128 v[190:193], v164 offset:32768
	ds_read_b128 v[194:197], v164 offset:34816
	ds_read_b128 v[198:201], v163 offset:36864
	ds_read_b128 v[202:205], v163 offset:38912
	ds_read_b128 v[206:209], v164 offset:36864
	ds_read_b128 v[210:213], v164 offset:38912
	s_add_u32 s46, s46, s22
	s_addc_u32 s47, s47, s23
	s_mov_b32 m0, s60
	s_nop 0
	global_load_lds_dwordx4 v146, s[46:47]
	s_mov_b32 m0, s61
	s_nop 0
	global_load_lds_dwordx4 v150, s[46:47]
	s_waitcnt lgkmcnt(8)
	ds_read_b128 v[214:217], v161 offset:49152
	ds_read_b128 v[218:221], v161 offset:51200
	ds_read_b128 v[222:225], v162 offset:49152
	ds_read_b128 v[226:229], v162 offset:51200
	s_waitcnt vmcnt(8)
	s_waitcnt lgkmcnt(0)
	s_barrier
	s_waitcnt lgkmcnt(0)
	s_setprio 1
	v_mfma_f32_16x16x128_f8f6f4 v[18:21], v[166:169], v[182:185], v[18:21] cbsz:4 blgp:4
	v_mfma_f32_16x16x128_f8f6f4 v[18:21], v[174:177], v[190:193], v[18:21] cbsz:4 blgp:4
	v_mfma_f32_16x16x128_f8f6f4 v[22:25], v[170:173], v[182:185], v[22:25] cbsz:4 blgp:4
	v_mfma_f32_16x16x128_f8f6f4 v[22:25], v[178:181], v[190:193], v[22:25] cbsz:4 blgp:4
	v_mfma_f32_16x16x128_f8f6f4 v[50:53], v[214:217], v[182:185], v[50:53] cbsz:4 blgp:4
	v_mfma_f32_16x16x128_f8f6f4 v[50:53], v[222:225], v[190:193], v[50:53] cbsz:4 blgp:4
	v_mfma_f32_16x16x128_f8f6f4 v[54:57], v[218:221], v[182:185], v[54:57] cbsz:4 blgp:4
	v_mfma_f32_16x16x128_f8f6f4 v[54:57], v[226:229], v[190:193], v[54:57] cbsz:4 blgp:4
	v_mfma_f32_16x16x128_f8f6f4 v[26:29], v[166:169], v[186:189], v[26:29] cbsz:4 blgp:4
	v_mfma_f32_16x16x128_f8f6f4 v[26:29], v[174:177], v[194:197], v[26:29] cbsz:4 blgp:4
	v_mfma_f32_16x16x128_f8f6f4 v[30:33], v[170:173], v[186:189], v[30:33] cbsz:4 blgp:4
	v_mfma_f32_16x16x128_f8f6f4 v[30:33], v[178:181], v[194:197], v[30:33] cbsz:4 blgp:4
	v_mfma_f32_16x16x128_f8f6f4 v[58:61], v[214:217], v[186:189], v[58:61] cbsz:4 blgp:4
	v_mfma_f32_16x16x128_f8f6f4 v[58:61], v[222:225], v[194:197], v[58:61] cbsz:4 blgp:4
	v_mfma_f32_16x16x128_f8f6f4 v[62:65], v[218:221], v[186:189], v[62:65] cbsz:4 blgp:4
	v_mfma_f32_16x16x128_f8f6f4 v[62:65], v[226:229], v[194:197], v[62:65] cbsz:4 blgp:4
	v_mfma_f32_16x16x128_f8f6f4 v[34:37], v[166:169], v[198:201], v[34:37] cbsz:4 blgp:4
	v_mfma_f32_16x16x128_f8f6f4 v[34:37], v[174:177], v[206:209], v[34:37] cbsz:4 blgp:4
	v_mfma_f32_16x16x128_f8f6f4 v[38:41], v[170:173], v[198:201], v[38:41] cbsz:4 blgp:4
	v_mfma_f32_16x16x128_f8f6f4 v[38:41], v[178:181], v[206:209], v[38:41] cbsz:4 blgp:4
	v_mfma_f32_16x16x128_f8f6f4 v[66:69], v[214:217], v[198:201], v[66:69] cbsz:4 blgp:4
	v_mfma_f32_16x16x128_f8f6f4 v[66:69], v[222:225], v[206:209], v[66:69] cbsz:4 blgp:4
	v_mfma_f32_16x16x128_f8f6f4 v[70:73], v[218:221], v[198:201], v[70:73] cbsz:4 blgp:4
	v_mfma_f32_16x16x128_f8f6f4 v[70:73], v[226:229], v[206:209], v[70:73] cbsz:4 blgp:4
	v_mfma_f32_16x16x128_f8f6f4 v[42:45], v[166:169], v[202:205], v[42:45] cbsz:4 blgp:4
	v_mfma_f32_16x16x128_f8f6f4 v[42:45], v[174:177], v[210:213], v[42:45] cbsz:4 blgp:4
	v_mfma_f32_16x16x128_f8f6f4 v[46:49], v[170:173], v[202:205], v[46:49] cbsz:4 blgp:4
	v_mfma_f32_16x16x128_f8f6f4 v[46:49], v[178:181], v[210:213], v[46:49] cbsz:4 blgp:4
	v_mfma_f32_16x16x128_f8f6f4 v[74:77], v[214:217], v[202:205], v[74:77] cbsz:4 blgp:4
	v_mfma_f32_16x16x128_f8f6f4 v[74:77], v[222:225], v[210:213], v[74:77] cbsz:4 blgp:4
	v_mfma_f32_16x16x128_f8f6f4 v[78:81], v[218:221], v[202:205], v[78:81] cbsz:4 blgp:4
	v_mfma_f32_16x16x128_f8f6f4 v[78:81], v[226:229], v[210:213], v[78:81] cbsz:4 blgp:4
	s_setprio 0
	s_barrier
	s_mov_b32 m0, s64
	s_nop 0
	global_load_lds_dwordx4 v148, s[42:43]
	s_mov_b32 m0, s65
	s_nop 0
	global_load_lds_dwordx4 v152, s[42:43]
	ds_read_b128 v[182:185], v163 offset:49152
	ds_read_b128 v[186:189], v163 offset:51200
	ds_read_b128 v[190:193], v164 offset:49152
	ds_read_b128 v[194:197], v164 offset:51200
	ds_read_b128 v[198:201], v163 offset:53248
	ds_read_b128 v[202:205], v163 offset:55296
	ds_read_b128 v[206:209], v164 offset:53248
	ds_read_b128 v[210:213], v164 offset:55296
	s_mov_b32 m0, s66
	s_nop 0
	global_load_lds_dwordx4 v146, s[44:45]
	s_mov_b32 m0, s67
	s_nop 0
	global_load_lds_dwordx4 v150, s[44:45]
	s_add_u32 s42, s42, s24
	s_addc_u32 s43, s43, s25
	s_mov_b32 m0, s68
	s_nop 0
	global_load_lds_dwordx4 v148, s[42:43]
	s_mov_b32 m0, s69
	s_nop 0
	global_load_lds_dwordx4 v152, s[42:43]
	s_waitcnt vmcnt(8)
	s_waitcnt lgkmcnt(0)
	s_barrier
	s_setprio 1
	v_mfma_f32_16x16x128_f8f6f4 v[86:89], v[166:169], v[182:185], v[86:89] cbsz:4 blgp:4
	v_mfma_f32_16x16x128_f8f6f4 v[86:89], v[174:177], v[190:193], v[86:89] cbsz:4 blgp:4
	v_mfma_f32_16x16x128_f8f6f4 v[90:93], v[170:173], v[182:185], v[90:93] cbsz:4 blgp:4
	v_mfma_f32_16x16x128_f8f6f4 v[90:93], v[178:181], v[190:193], v[90:93] cbsz:4 blgp:4
	v_mfma_f32_16x16x128_f8f6f4 v[94:97], v[214:217], v[182:185], v[94:97] cbsz:4 blgp:4
	v_mfma_f32_16x16x128_f8f6f4 v[94:97], v[222:225], v[190:193], v[94:97] cbsz:4 blgp:4
	v_mfma_f32_16x16x128_f8f6f4 v[102:105], v[218:221], v[182:185], v[102:105] cbsz:4 blgp:4
	v_mfma_f32_16x16x128_f8f6f4 v[102:105], v[226:229], v[190:193], v[102:105] cbsz:4 blgp:4
	v_mfma_f32_16x16x128_f8f6f4 v[98:101], v[166:169], v[186:189], v[98:101] cbsz:4 blgp:4
	v_mfma_f32_16x16x128_f8f6f4 v[98:101], v[174:177], v[194:197], v[98:101] cbsz:4 blgp:4
	v_mfma_f32_16x16x128_f8f6f4 v[106:109], v[170:173], v[186:189], v[106:109] cbsz:4 blgp:4
	v_mfma_f32_16x16x128_f8f6f4 v[106:109], v[178:181], v[194:197], v[106:109] cbsz:4 blgp:4
	v_mfma_f32_16x16x128_f8f6f4 v[110:113], v[214:217], v[186:189], v[110:113] cbsz:4 blgp:4
	v_mfma_f32_16x16x128_f8f6f4 v[110:113], v[222:225], v[194:197], v[110:113] cbsz:4 blgp:4
	v_mfma_f32_16x16x128_f8f6f4 v[114:117], v[218:221], v[186:189], v[114:117] cbsz:4 blgp:4
	v_mfma_f32_16x16x128_f8f6f4 v[114:117], v[226:229], v[194:197], v[114:117] cbsz:4 blgp:4
	v_mfma_f32_16x16x128_f8f6f4 v[118:121], v[166:169], v[198:201], v[118:121] cbsz:4 blgp:4
	v_mfma_f32_16x16x128_f8f6f4 v[118:121], v[174:177], v[206:209], v[118:121] cbsz:4 blgp:4
	v_mfma_f32_16x16x128_f8f6f4 v[126:129], v[170:173], v[198:201], v[126:129] cbsz:4 blgp:4
	v_mfma_f32_16x16x128_f8f6f4 v[126:129], v[178:181], v[206:209], v[126:129] cbsz:4 blgp:4
	v_mfma_f32_16x16x128_f8f6f4 v[122:125], v[214:217], v[198:201], v[122:125] cbsz:4 blgp:4
	v_mfma_f32_16x16x128_f8f6f4 v[122:125], v[222:225], v[206:209], v[122:125] cbsz:4 blgp:4
	v_mfma_f32_16x16x128_f8f6f4 v[130:133], v[218:221], v[198:201], v[130:133] cbsz:4 blgp:4
	v_mfma_f32_16x16x128_f8f6f4 v[130:133], v[226:229], v[206:209], v[130:133] cbsz:4 blgp:4
	v_mfma_f32_16x16x128_f8f6f4 v[138:141], v[166:169], v[202:205], v[138:141] cbsz:4 blgp:4
	v_mfma_f32_16x16x128_f8f6f4 v[138:141], v[174:177], v[210:213], v[138:141] cbsz:4 blgp:4
	v_mfma_f32_16x16x128_f8f6f4 v[82:85], v[170:173], v[202:205], v[82:85] cbsz:4 blgp:4
	v_mfma_f32_16x16x128_f8f6f4 v[82:85], v[178:181], v[210:213], v[82:85] cbsz:4 blgp:4
	v_mfma_f32_16x16x128_f8f6f4 v[134:137], v[214:217], v[202:205], v[134:137] cbsz:4 blgp:4
	v_mfma_f32_16x16x128_f8f6f4 v[134:137], v[222:225], v[210:213], v[134:137] cbsz:4 blgp:4
	v_mfma_f32_16x16x128_f8f6f4 v[142:145], v[218:221], v[202:205], v[142:145] cbsz:4 blgp:4
	v_mfma_f32_16x16x128_f8f6f4 v[142:145], v[226:229], v[210:213], v[142:145] cbsz:4 blgp:4
	s_setprio 0
	s_andn2_b64 vcc, exec, s[34:35]
	s_barrier
	s_cbranch_vccnz .LBB4_4
	s_ashr_i32 s29, s28, 31
	s_lshl_b64 s[42:43], s[28:29], 10
	s_add_u32 s42, s10, s42
	s_addc_u32 s43, s11, s43
	s_add_u32 s29, s40, 0x200
	s_addc_u32 s78, s41, 0
	s_add_u32 s79, s38, 0x200
	s_addc_u32 s80, s39, 0
	s_add_u32 s38, s81, 0x180
	s_addc_u32 s39, s82, 0
	s_mov_b32 s81, 4
	s_cmp_eq_u32 s63, s81
	s_cselect_b64 s[40:41], -1, 0
	s_cmp_lg_u32 s63, s81
	s_cbranch_scc1 .LBB4_15

.Llast_4:
	ds_read_b128 v[166:169], v161
	ds_read_b128 v[170:173], v161 offset:2048
	ds_read_b128 v[174:177], v162
	ds_read_b128 v[178:181], v162 offset:2048
	s_and_b64 s[40:41], s[40:41], exec
	s_cselect_b32 s46, s36, s29
	s_cselect_b32 s47, s37, s78
	s_cselect_b32 s49, s5, s80
	s_cselect_b32 s48, s4, s79
	s_add_u32 s44, s46, 0x80
	s_addc_u32 s45, s47, 0
	s_add_u32 s40, s48, 0x80
	s_addc_u32 s41, s49, 0
	ds_read_b128 v[182:185], v163
	ds_read_b128 v[186:189], v163 offset:2048
	ds_read_b128 v[190:193], v164
	ds_read_b128 v[194:197], v164 offset:2048
	ds_read_b128 v[198:201], v163 offset:4096
	ds_read_b128 v[202:205], v163 offset:6144
	ds_read_b128 v[206:209], v164 offset:4096
	ds_read_b128 v[210:213], v164 offset:6144
	s_mov_b32 m0, s70
	s_nop 0
	global_load_lds_dwordx4 v146, s[38:39]
	s_mov_b32 m0, s71
	s_nop 0
	global_load_lds_dwordx4 v150, s[38:39]
	s_waitcnt lgkmcnt(8)
	ds_read_b128 v[214:217], v161 offset:16384
	ds_read_b128 v[218:221], v161 offset:18432
	ds_read_b128 v[222:225], v162 offset:16384
	ds_read_b128 v[226:229], v162 offset:18432
	s_waitcnt vmcnt(12)
	s_waitcnt lgkmcnt(0)
	s_barrier
	s_waitcnt lgkmcnt(0)
	s_setprio 1
	v_mfma_f32_16x16x128_f8f6f4 v[18:21], v[166:169], v[182:185], v[18:21] cbsz:4 blgp:4
	v_mfma_f32_16x16x128_f8f6f4 v[18:21], v[174:177], v[190:193], v[18:21] cbsz:4 blgp:4
	v_mfma_f32_16x16x128_f8f6f4 v[22:25], v[170:173], v[182:185], v[22:25] cbsz:4 blgp:4
	v_mfma_f32_16x16x128_f8f6f4 v[22:25], v[178:181], v[190:193], v[22:25] cbsz:4 blgp:4
	v_mfma_f32_16x16x128_f8f6f4 v[50:53], v[214:217], v[182:185], v[50:53] cbsz:4 blgp:4
	v_mfma_f32_16x16x128_f8f6f4 v[50:53], v[222:225], v[190:193], v[50:53] cbsz:4 blgp:4
	v_mfma_f32_16x16x128_f8f6f4 v[54:57], v[218:221], v[182:185], v[54:57] cbsz:4 blgp:4
	v_mfma_f32_16x16x128_f8f6f4 v[54:57], v[226:229], v[190:193], v[54:57] cbsz:4 blgp:4
	v_mfma_f32_16x16x128_f8f6f4 v[26:29], v[166:169], v[186:189], v[26:29] cbsz:4 blgp:4
	v_mfma_f32_16x16x128_f8f6f4 v[26:29], v[174:177], v[194:197], v[26:29] cbsz:4 blgp:4
	v_mfma_f32_16x16x128_f8f6f4 v[30:33], v[170:173], v[186:189], v[30:33] cbsz:4 blgp:4
	v_mfma_f32_16x16x128_f8f6f4 v[30:33], v[178:181], v[194:197], v[30:33] cbsz:4 blgp:4
	v_mfma_f32_16x16x128_f8f6f4 v[58:61], v[214:217], v[186:189], v[58:61] cbsz:4 blgp:4
	v_mfma_f32_16x16x128_f8f6f4 v[58:61], v[222:225], v[194:197], v[58:61] cbsz:4 blgp:4
	v_mfma_f32_16x16x128_f8f6f4 v[62:65], v[218:221], v[186:189], v[62:65] cbsz:4 blgp:4
	v_mfma_f32_16x16x128_f8f6f4 v[62:65], v[226:229], v[194:197], v[62:65] cbsz:4 blgp:4
	v_mfma_f32_16x16x128_f8f6f4 v[34:37], v[166:169], v[198:201], v[34:37] cbsz:4 blgp:4
	v_mfma_f32_16x16x128_f8f6f4 v[34:37], v[174:177], v[206:209], v[34:37] cbsz:4 blgp:4
	v_mfma_f32_16x16x128_f8f6f4 v[38:41], v[170:173], v[198:201], v[38:41] cbsz:4 blgp:4
	v_mfma_f32_16x16x128_f8f6f4 v[38:41], v[178:181], v[206:209], v[38:41] cbsz:4 blgp:4
	v_mfma_f32_16x16x128_f8f6f4 v[66:69], v[214:217], v[198:201], v[66:69] cbsz:4 blgp:4
	v_mfma_f32_16x16x128_f8f6f4 v[66:69], v[222:225], v[206:209], v[66:69] cbsz:4 blgp:4
	v_mfma_f32_16x16x128_f8f6f4 v[70:73], v[218:221], v[198:201], v[70:73] cbsz:4 blgp:4
	v_mfma_f32_16x16x128_f8f6f4 v[70:73], v[226:229], v[206:209], v[70:73] cbsz:4 blgp:4
	v_mfma_f32_16x16x128_f8f6f4 v[42:45], v[166:169], v[202:205], v[42:45] cbsz:4 blgp:4
	v_mfma_f32_16x16x128_f8f6f4 v[42:45], v[174:177], v[210:213], v[42:45] cbsz:4 blgp:4
	v_mfma_f32_16x16x128_f8f6f4 v[46:49], v[170:173], v[202:205], v[46:49] cbsz:4 blgp:4
	v_mfma_f32_16x16x128_f8f6f4 v[46:49], v[178:181], v[210:213], v[46:49] cbsz:4 blgp:4
	v_mfma_f32_16x16x128_f8f6f4 v[74:77], v[214:217], v[202:205], v[74:77] cbsz:4 blgp:4
	v_mfma_f32_16x16x128_f8f6f4 v[74:77], v[222:225], v[210:213], v[74:77] cbsz:4 blgp:4
	v_mfma_f32_16x16x128_f8f6f4 v[78:81], v[218:221], v[202:205], v[78:81] cbsz:4 blgp:4
	v_mfma_f32_16x16x128_f8f6f4 v[78:81], v[226:229], v[210:213], v[78:81] cbsz:4 blgp:4
	s_setprio 0
	s_barrier
	s_mov_b32 m0, s55
	s_nop 0
	global_load_lds_dwordx4 v148, s[48:49]
	s_mov_b32 m0, s56
	s_nop 0
	global_load_lds_dwordx4 v152, s[48:49]
	ds_read_b128 v[182:185], v163 offset:16384
	ds_read_b128 v[186:189], v163 offset:18432
	ds_read_b128 v[190:193], v164 offset:16384
	ds_read_b128 v[194:197], v164 offset:18432
	ds_read_b128 v[198:201], v163 offset:20480
	ds_read_b128 v[202:205], v163 offset:22528
	ds_read_b128 v[206:209], v164 offset:20480
	ds_read_b128 v[210:213], v164 offset:22528
	s_mov_b32 m0, s54
	s_nop 0
	global_load_lds_dwordx4 v146, s[46:47]
	s_mov_b32 m0, s57
	s_nop 0
	global_load_lds_dwordx4 v150, s[46:47]
	s_add_u32 s48, s48, s24
	s_addc_u32 s49, s49, s25
	s_mov_b32 m0, s58
	s_nop 0
	global_load_lds_dwordx4 v148, s[48:49]
	s_mov_b32 m0, s59
	s_nop 0
	global_load_lds_dwordx4 v152, s[48:49]
	s_waitcnt vmcnt(8)
	s_waitcnt lgkmcnt(0)
	s_barrier
	s_setprio 1
	v_mfma_f32_16x16x128_f8f6f4 v[86:89], v[166:169], v[182:185], v[86:89] cbsz:4 blgp:4
	v_mfma_f32_16x16x128_f8f6f4 v[86:89], v[174:177], v[190:193], v[86:89] cbsz:4 blgp:4
	v_mfma_f32_16x16x128_f8f6f4 v[90:93], v[170:173], v[182:185], v[90:93] cbsz:4 blgp:4
	v_mfma_f32_16x16x128_f8f6f4 v[90:93], v[178:181], v[190:193], v[90:93] cbsz:4 blgp:4
	v_mfma_f32_16x16x128_f8f6f4 v[94:97], v[214:217], v[182:185], v[94:97] cbsz:4 blgp:4
	v_mfma_f32_16x16x128_f8f6f4 v[94:97], v[222:225], v[190:193], v[94:97] cbsz:4 blgp:4
	v_mfma_f32_16x16x128_f8f6f4 v[102:105], v[218:221], v[182:185], v[102:105] cbsz:4 blgp:4
	v_mfma_f32_16x16x128_f8f6f4 v[102:105], v[226:229], v[190:193], v[102:105] cbsz:4 blgp:4
	v_mfma_f32_16x16x128_f8f6f4 v[98:101], v[166:169], v[186:189], v[98:101] cbsz:4 blgp:4
	v_mfma_f32_16x16x128_f8f6f4 v[98:101], v[174:177], v[194:197], v[98:101] cbsz:4 blgp:4
	v_mfma_f32_16x16x128_f8f6f4 v[106:109], v[170:173], v[186:189], v[106:109] cbsz:4 blgp:4
	v_mfma_f32_16x16x128_f8f6f4 v[106:109], v[178:181], v[194:197], v[106:109] cbsz:4 blgp:4
	v_mfma_f32_16x16x128_f8f6f4 v[110:113], v[214:217], v[186:189], v[110:113] cbsz:4 blgp:4
	v_mfma_f32_16x16x128_f8f6f4 v[110:113], v[222:225], v[194:197], v[110:113] cbsz:4 blgp:4
	v_mfma_f32_16x16x128_f8f6f4 v[114:117], v[218:221], v[186:189], v[114:117] cbsz:4 blgp:4
	v_mfma_f32_16x16x128_f8f6f4 v[114:117], v[226:229], v[194:197], v[114:117] cbsz:4 blgp:4
	v_mfma_f32_16x16x128_f8f6f4 v[118:121], v[166:169], v[198:201], v[118:121] cbsz:4 blgp:4
	v_mfma_f32_16x16x128_f8f6f4 v[118:121], v[174:177], v[206:209], v[118:121] cbsz:4 blgp:4
	v_mfma_f32_16x16x128_f8f6f4 v[126:129], v[170:173], v[198:201], v[126:129] cbsz:4 blgp:4
	v_mfma_f32_16x16x128_f8f6f4 v[126:129], v[178:181], v[206:209], v[126:129] cbsz:4 blgp:4
	v_mfma_f32_16x16x128_f8f6f4 v[122:125], v[214:217], v[198:201], v[122:125] cbsz:4 blgp:4
	v_mfma_f32_16x16x128_f8f6f4 v[122:125], v[222:225], v[206:209], v[122:125] cbsz:4 blgp:4
	v_mfma_f32_16x16x128_f8f6f4 v[130:133], v[218:221], v[198:201], v[130:133] cbsz:4 blgp:4
	v_mfma_f32_16x16x128_f8f6f4 v[130:133], v[226:229], v[206:209], v[130:133] cbsz:4 blgp:4
	v_mfma_f32_16x16x128_f8f6f4 v[138:141], v[166:169], v[202:205], v[138:141] cbsz:4 blgp:4
	v_mfma_f32_16x16x128_f8f6f4 v[138:141], v[174:177], v[210:213], v[138:141] cbsz:4 blgp:4
	v_mfma_f32_16x16x128_f8f6f4 v[82:85], v[170:173], v[202:205], v[82:85] cbsz:4 blgp:4
	v_mfma_f32_16x16x128_f8f6f4 v[82:85], v[178:181], v[210:213], v[82:85] cbsz:4 blgp:4
	v_mfma_f32_16x16x128_f8f6f4 v[134:137], v[214:217], v[202:205], v[134:137] cbsz:4 blgp:4
	v_mfma_f32_16x16x128_f8f6f4 v[134:137], v[222:225], v[210:213], v[134:137] cbsz:4 blgp:4
	v_mfma_f32_16x16x128_f8f6f4 v[142:145], v[218:221], v[202:205], v[142:145] cbsz:4 blgp:4
	v_mfma_f32_16x16x128_f8f6f4 v[142:145], v[226:229], v[210:213], v[142:145] cbsz:4 blgp:4
	s_setprio 0
	s_barrier
	ds_read_b128 v[166:169], v161 offset:32768
	ds_read_b128 v[170:173], v161 offset:34816
	ds_read_b128 v[174:177], v162 offset:32768
	ds_read_b128 v[178:181], v162 offset:34816
	ds_read_b128 v[182:185], v163 offset:32768
	ds_read_b128 v[186:189], v163 offset:34816
	ds_read_b128 v[190:193], v164 offset:32768
	ds_read_b128 v[194:197], v164 offset:34816
	ds_read_b128 v[198:201], v163 offset:36864
	ds_read_b128 v[202:205], v163 offset:38912
	ds_read_b128 v[206:209], v164 offset:36864
	ds_read_b128 v[210:213], v164 offset:38912
	s_add_u32 s46, s46, s22
	s_addc_u32 s47, s47, s23
	s_mov_b32 m0, s60
	s_nop 0
	global_load_lds_dwordx4 v146, s[46:47]
	s_mov_b32 m0, s61
	s_nop 0
	global_load_lds_dwordx4 v150, s[46:47]
	s_waitcnt lgkmcnt(8)
	ds_read_b128 v[214:217], v161 offset:49152
	ds_read_b128 v[218:221], v161 offset:51200
	ds_read_b128 v[222:225], v162 offset:49152
	ds_read_b128 v[226:229], v162 offset:51200
	s_waitcnt vmcnt(8)
	s_waitcnt lgkmcnt(0)
	s_barrier
	s_waitcnt lgkmcnt(0)
	s_setprio 1
	v_mfma_f32_16x16x128_f8f6f4 v[18:21], v[166:169], v[182:185], v[18:21] cbsz:4 blgp:4
	v_mfma_f32_16x16x128_f8f6f4 v[18:21], v[174:177], v[190:193], v[18:21] cbsz:4 blgp:4
	v_mfma_f32_16x16x128_f8f6f4 v[22:25], v[170:173], v[182:185], v[22:25] cbsz:4 blgp:4
	v_mfma_f32_16x16x128_f8f6f4 v[22:25], v[178:181], v[190:193], v[22:25] cbsz:4 blgp:4
	v_mfma_f32_16x16x128_f8f6f4 v[50:53], v[214:217], v[182:185], v[50:53] cbsz:4 blgp:4
	v_mfma_f32_16x16x128_f8f6f4 v[50:53], v[222:225], v[190:193], v[50:53] cbsz:4 blgp:4
	v_mfma_f32_16x16x128_f8f6f4 v[54:57], v[218:221], v[182:185], v[54:57] cbsz:4 blgp:4
	v_mfma_f32_16x16x128_f8f6f4 v[54:57], v[226:229], v[190:193], v[54:57] cbsz:4 blgp:4
	v_mfma_f32_16x16x128_f8f6f4 v[26:29], v[166:169], v[186:189], v[26:29] cbsz:4 blgp:4
	v_mfma_f32_16x16x128_f8f6f4 v[26:29], v[174:177], v[194:197], v[26:29] cbsz:4 blgp:4
	v_mfma_f32_16x16x128_f8f6f4 v[30:33], v[170:173], v[186:189], v[30:33] cbsz:4 blgp:4
	v_mfma_f32_16x16x128_f8f6f4 v[30:33], v[178:181], v[194:197], v[30:33] cbsz:4 blgp:4
	v_mfma_f32_16x16x128_f8f6f4 v[58:61], v[214:217], v[186:189], v[58:61] cbsz:4 blgp:4
	v_mfma_f32_16x16x128_f8f6f4 v[58:61], v[222:225], v[194:197], v[58:61] cbsz:4 blgp:4
	v_mfma_f32_16x16x128_f8f6f4 v[62:65], v[218:221], v[186:189], v[62:65] cbsz:4 blgp:4
	v_mfma_f32_16x16x128_f8f6f4 v[62:65], v[226:229], v[194:197], v[62:65] cbsz:4 blgp:4
	v_mfma_f32_16x16x128_f8f6f4 v[34:37], v[166:169], v[198:201], v[34:37] cbsz:4 blgp:4
	v_mfma_f32_16x16x128_f8f6f4 v[34:37], v[174:177], v[206:209], v[34:37] cbsz:4 blgp:4
	v_mfma_f32_16x16x128_f8f6f4 v[38:41], v[170:173], v[198:201], v[38:41] cbsz:4 blgp:4
	v_mfma_f32_16x16x128_f8f6f4 v[38:41], v[178:181], v[206:209], v[38:41] cbsz:4 blgp:4
	v_mfma_f32_16x16x128_f8f6f4 v[66:69], v[214:217], v[198:201], v[66:69] cbsz:4 blgp:4
	v_mfma_f32_16x16x128_f8f6f4 v[66:69], v[222:225], v[206:209], v[66:69] cbsz:4 blgp:4
	v_mfma_f32_16x16x128_f8f6f4 v[70:73], v[218:221], v[198:201], v[70:73] cbsz:4 blgp:4
	v_mfma_f32_16x16x128_f8f6f4 v[70:73], v[226:229], v[206:209], v[70:73] cbsz:4 blgp:4
	v_mfma_f32_16x16x128_f8f6f4 v[42:45], v[166:169], v[202:205], v[42:45] cbsz:4 blgp:4
	v_mfma_f32_16x16x128_f8f6f4 v[42:45], v[174:177], v[210:213], v[42:45] cbsz:4 blgp:4
	v_mfma_f32_16x16x128_f8f6f4 v[46:49], v[170:173], v[202:205], v[46:49] cbsz:4 blgp:4
	v_mfma_f32_16x16x128_f8f6f4 v[46:49], v[178:181], v[210:213], v[46:49] cbsz:4 blgp:4
	v_mfma_f32_16x16x128_f8f6f4 v[74:77], v[214:217], v[202:205], v[74:77] cbsz:4 blgp:4
	v_mfma_f32_16x16x128_f8f6f4 v[74:77], v[222:225], v[210:213], v[74:77] cbsz:4 blgp:4
	v_mfma_f32_16x16x128_f8f6f4 v[78:81], v[218:221], v[202:205], v[78:81] cbsz:4 blgp:4
	v_mfma_f32_16x16x128_f8f6f4 v[78:81], v[226:229], v[210:213], v[78:81] cbsz:4 blgp:4
	s_setprio 0
	s_barrier
	s_mov_b32 m0, s64
	s_nop 0
	global_load_lds_dwordx4 v148, s[40:41]
	s_mov_b32 m0, s65
	s_nop 0
	global_load_lds_dwordx4 v152, s[40:41]
	ds_read_b128 v[182:185], v163 offset:49152
	ds_read_b128 v[186:189], v163 offset:51200
	ds_read_b128 v[190:193], v164 offset:49152
	ds_read_b128 v[194:197], v164 offset:51200
	ds_read_b128 v[198:201], v163 offset:53248
	ds_read_b128 v[202:205], v163 offset:55296
	ds_read_b128 v[206:209], v164 offset:53248
	ds_read_b128 v[210:213], v164 offset:55296
	s_mov_b32 m0, s66
	s_nop 0
	global_load_lds_dwordx4 v146, s[44:45]
	s_mov_b32 m0, s67
	s_nop 0
	global_load_lds_dwordx4 v150, s[44:45]
	s_add_u32 s40, s40, s24
	s_addc_u32 s41, s41, s25
	s_mov_b32 m0, s68
	s_nop 0
	global_load_lds_dwordx4 v148, s[40:41]
	s_mov_b32 m0, s69
	s_nop 0
	global_load_lds_dwordx4 v152, s[40:41]
	s_waitcnt vmcnt(8)
	s_waitcnt lgkmcnt(0)
	s_barrier
	s_setprio 1
	v_mfma_f32_16x16x128_f8f6f4 v[86:89], v[166:169], v[182:185], v[86:89] cbsz:4 blgp:4
	v_med3_f32 v232, v18, v160, 0
	v_med3_f32 v230, v19, v160, 0
	v_med3_f32 v233, v20, v160, 0
	v_mfma_f32_16x16x128_f8f6f4 v[86:89], v[174:177], v[190:193], v[86:89] cbsz:4 blgp:4
	v_med3_f32 v234, v21, v160, 0
	v_cvt_scalef32_pk_fp4_f32 v232, v232, v230, v159
	v_med3_f32 v235, v22, v160, 0
	v_med3_f32 v236, v23, v160, 0
	v_mfma_f32_16x16x128_f8f6f4 v[90:93], v[170:173], v[182:185], v[90:93] cbsz:4 blgp:4
	v_cvt_scalef32_pk_fp4_f32 v232, v233, v234, v159 op_sel:[0,0,1,0]
	v_med3_f32 v233, v50, v160, 0
	v_med3_f32 v230, v51, v160, 0
	v_mfma_f32_16x16x128_f8f6f4 v[90:93], v[178:181], v[190:193], v[90:93] cbsz:4 blgp:4
	v_med3_f32 v237, v24, v160, 0
	v_med3_f32 v238, v25, v160, 0
	v_cvt_scalef32_pk_fp4_f32 v232, v235, v236, v159 op_sel:[0,0,0,1]
	v_med3_f32 v234, v52, v160, 0
	v_mfma_f32_16x16x128_f8f6f4 v[94:97], v[214:217], v[182:185], v[94:97] cbsz:4 blgp:4
	v_med3_f32 v235, v53, v160, 0
	v_cvt_scalef32_pk_fp4_f32 v233, v233, v230, v159
	v_cvt_scalef32_pk_fp4_f32 v232, v237, v238, v159 op_sel:[0,0,1,1]
	v_mfma_f32_16x16x128_f8f6f4 v[94:97], v[222:225], v[190:193], v[94:97] cbsz:4 blgp:4
	v_med3_f32 v236, v54, v160, 0
	v_med3_f32 v237, v55, v160, 0
	v_cvt_scalef32_pk_fp4_f32 v233, v234, v235, v159 op_sel:[0,0,1,0]
	v_med3_f32 v234, v26, v160, 0
	v_mfma_f32_16x16x128_f8f6f4 v[102:105], v[218:221], v[182:185], v[102:105] cbsz:4 blgp:4
	v_med3_f32 v230, v27, v160, 0
	v_med3_f32 v238, v56, v160, 0
	v_med3_f32 v239, v57, v160, 0
	v_mfma_f32_16x16x128_f8f6f4 v[102:105], v[226:229], v[190:193], v[102:105] cbsz:4 blgp:4
	v_cvt_scalef32_pk_fp4_f32 v233, v236, v237, v159 op_sel:[0,0,0,1]
	v_med3_f32 v235, v28, v160, 0
	v_med3_f32 v236, v29, v160, 0
	v_cvt_scalef32_pk_fp4_f32 v234, v234, v230, v159
	v_mfma_f32_16x16x128_f8f6f4 v[98:101], v[166:169], v[186:189], v[98:101] cbsz:4 blgp:4
	v_cvt_scalef32_pk_fp4_f32 v233, v238, v239, v159 op_sel:[0,0,1,1]
	v_med3_f32 v237, v30, v160, 0
	v_med3_f32 v238, v31, v160, 0
	v_mfma_f32_16x16x128_f8f6f4 v[98:101], v[174:177], v[194:197], v[98:101] cbsz:4 blgp:4
	v_cvt_scalef32_pk_fp4_f32 v234, v235, v236, v159 op_sel:[0,0,1,0]
	v_med3_f32 v235, v58, v160, 0
	v_med3_f32 v230, v59, v160, 0
	v_med3_f32 v239, v32, v160, 0
	v_mfma_f32_16x16x128_f8f6f4 v[106:109], v[170:173], v[186:189], v[106:109] cbsz:4 blgp:4
	v_med3_f32 v240, v33, v160, 0
	v_cvt_scalef32_pk_fp4_f32 v234, v237, v238, v159 op_sel:[0,0,0,1]
	v_med3_f32 v236, v60, v160, 0
	v_mfma_f32_16x16x128_f8f6f4 v[106:109], v[178:181], v[194:197], v[106:109] cbsz:4 blgp:4
	v_med3_f32 v237, v61, v160, 0
	v_cvt_scalef32_pk_fp4_f32 v235, v235, v230, v159
	v_lshl_add_u32 v244, s77, 8, v149
	v_lshl_or_b32 v246, s76, 8, v151
	v_mfma_f32_16x16x128_f8f6f4 v[110:113], v[214:217], v[186:189], v[110:113] cbsz:4 blgp:4
	v_cvt_scalef32_pk_fp4_f32 v234, v239, v240, v159 op_sel:[0,0,1,1]
	v_med3_f32 v238, v62, v160, 0
	v_med3_f32 v239, v63, v160, 0
	v_mfma_f32_16x16x128_f8f6f4 v[110:113], v[222:225], v[194:197], v[110:113] cbsz:4 blgp:4
	v_cvt_scalef32_pk_fp4_f32 v235, v236, v237, v159 op_sel:[0,0,1,0]
	v_ashrrev_i32_e32 v246, 1, v246
	v_med3_f32 v240, v64, v160, 0
	v_med3_f32 v241, v65, v160, 0
	v_mfma_f32_16x16x128_f8f6f4 v[114:117], v[218:221], v[186:189], v[114:117] cbsz:4 blgp:4
	v_cvt_scalef32_pk_fp4_f32 v235, v238, v239, v159 op_sel:[0,0,0,1]
	v_or_b32_e32 v230, v244, v153
	v_mov_b64_e32 v[236:237], s[8:9]
	v_mfma_f32_16x16x128_f8f6f4 v[114:117], v[226:229], v[194:197], v[114:117] cbsz:4 blgp:4
	v_ashrrev_i32_e32 v247, 31, v246
	v_cvt_scalef32_pk_fp4_f32 v235, v240, v241, v159 op_sel:[0,0,1,1]
	v_mad_i64_i32 v[238:239], s[84:85], v230, s12, v[236:237]
	v_permlane16_swap_b32_e32 v232, v234
	v_mfma_f32_16x16x128_f8f6f4 v[118:121], v[166:169], v[198:201], v[118:121] cbsz:4 blgp:4
	v_permlane16_swap_b32_e32 v233, v235
	v_lshl_add_u64 v[238:239], v[238:239], 0, v[246:247]
	global_store_dwordx4 v[238:239], v[232:235], off
	v_med3_f32 v230, v35, v160, 0
	v_mfma_f32_16x16x128_f8f6f4 v[118:121], v[174:177], v[206:209], v[118:121] cbsz:4 blgp:4
	v_med3_f32 v238, v39, v160, 0
	v_med3_f32 v232, v34, v160, 0
	v_med3_f32 v233, v36, v160, 0
	v_mfma_f32_16x16x128_f8f6f4 v[126:129], v[170:173], v[198:201], v[126:129] cbsz:4 blgp:4
	v_med3_f32 v234, v37, v160, 0
	v_cvt_scalef32_pk_fp4_f32 v232, v232, v230, v159
	v_med3_f32 v235, v38, v160, 0
	v_cvt_scalef32_pk_fp4_f32 v232, v233, v234, v159 op_sel:[0,0,1,0]
	v_mfma_f32_16x16x128_f8f6f4 v[126:129], v[178:181], v[206:209], v[126:129] cbsz:4 blgp:4
	v_med3_f32 v233, v66, v160, 0
	v_med3_f32 v230, v67, v160, 0
	v_med3_f32 v239, v40, v160, 0
	v_mfma_f32_16x16x128_f8f6f4 v[122:125], v[214:217], v[198:201], v[122:125] cbsz:4 blgp:4
	v_med3_f32 v240, v41, v160, 0
	v_cvt_scalef32_pk_fp4_f32 v232, v235, v238, v159 op_sel:[0,0,0,1]
	v_med3_f32 v234, v68, v160, 0
	v_med3_f32 v235, v69, v160, 0
	v_mfma_f32_16x16x128_f8f6f4 v[122:125], v[222:225], v[206:209], v[122:125] cbsz:4 blgp:4
	v_cvt_scalef32_pk_fp4_f32 v233, v233, v230, v159
	v_cvt_scalef32_pk_fp4_f32 v232, v239, v240, v159 op_sel:[0,0,1,1]
	v_med3_f32 v238, v70, v160, 0
	v_mfma_f32_16x16x128_f8f6f4 v[130:133], v[218:221], v[198:201], v[130:133] cbsz:4 blgp:4
	v_med3_f32 v239, v71, v160, 0
	v_cvt_scalef32_pk_fp4_f32 v233, v234, v235, v159 op_sel:[0,0,1,0]
	v_med3_f32 v234, v42, v160, 0
	v_med3_f32 v230, v43, v160, 0
	v_mfma_f32_16x16x128_f8f6f4 v[130:133], v[226:229], v[206:209], v[130:133] cbsz:4 blgp:4
	v_med3_f32 v240, v72, v160, 0
	v_med3_f32 v241, v73, v160, 0
	v_cvt_scalef32_pk_fp4_f32 v233, v238, v239, v159 op_sel:[0,0,0,1]
	v_mfma_f32_16x16x128_f8f6f4 v[138:141], v[166:169], v[202:205], v[138:141] cbsz:4 blgp:4
	v_med3_f32 v235, v44, v160, 0
	v_med3_f32 v238, v45, v160, 0
	v_cvt_scalef32_pk_fp4_f32 v234, v234, v230, v159
	v_cvt_scalef32_pk_fp4_f32 v233, v240, v241, v159 op_sel:[0,0,1,1]
	v_mfma_f32_16x16x128_f8f6f4 v[138:141], v[174:177], v[210:213], v[138:141] cbsz:4 blgp:4
	v_med3_f32 v239, v46, v160, 0
	v_med3_f32 v240, v47, v160, 0
	v_cvt_scalef32_pk_fp4_f32 v234, v235, v238, v159 op_sel:[0,0,1,0]
	v_mfma_f32_16x16x128_f8f6f4 v[82:85], v[170:173], v[202:205], v[82:85] cbsz:4 blgp:4
	v_med3_f32 v235, v74, v160, 0
	v_med3_f32 v230, v75, v160, 0
	v_med3_f32 v241, v48, v160, 0
	v_med3_f32 v242, v49, v160, 0
	v_mfma_f32_16x16x128_f8f6f4 v[82:85], v[178:181], v[210:213], v[82:85] cbsz:4 blgp:4
	v_cvt_scalef32_pk_fp4_f32 v234, v239, v240, v159 op_sel:[0,0,0,1]
	v_med3_f32 v238, v76, v160, 0
	v_med3_f32 v239, v77, v160, 0
	v_mfma_f32_16x16x128_f8f6f4 v[134:137], v[214:217], v[202:205], v[134:137] cbsz:4 blgp:4
	v_cvt_scalef32_pk_fp4_f32 v235, v235, v230, v159
	v_cvt_scalef32_pk_fp4_f32 v234, v241, v242, v159 op_sel:[0,0,1,1]
	v_med3_f32 v240, v78, v160, 0
	v_med3_f32 v241, v79, v160, 0
	v_mfma_f32_16x16x128_f8f6f4 v[134:137], v[222:225], v[210:213], v[134:137] cbsz:4 blgp:4
	v_cvt_scalef32_pk_fp4_f32 v235, v238, v239, v159 op_sel:[0,0,1,0]
	v_med3_f32 v242, v80, v160, 0
	v_med3_f32 v243, v81, v160, 0
	v_mfma_f32_16x16x128_f8f6f4 v[142:145], v[218:221], v[202:205], v[142:145] cbsz:4 blgp:4
	v_cvt_scalef32_pk_fp4_f32 v235, v240, v241, v159 op_sel:[0,0,0,1]
	v_or_b32_e32 v230, v244, v158
	v_cvt_scalef32_pk_fp4_f32 v235, v242, v243, v159 op_sel:[0,0,1,1]
	v_mad_i64_i32 v[238:239], s[84:85], v230, s12, v[236:237]
	v_mfma_f32_16x16x128_f8f6f4 v[142:145], v[226:229], v[210:213], v[142:145] cbsz:4 blgp:4
	v_permlane16_swap_b32_e32 v232, v234
	v_permlane16_swap_b32_e32 v233, v235
	v_lshl_add_u64 v[238:239], v[238:239], 0, v[246:247]
	global_store_dwordx4 v[238:239], v[232:235], off
	s_setprio 0
	s_add_i32 s40, s81, 2
	s_add_u32 s29, s29, 0x100
	s_addc_u32 s78, s78, 0
	s_add_u32 s79, s79, 0x100
	s_addc_u32 s80, s80, 0
	s_add_u32 s38, s38, 0x100
	s_addc_u32 s39, s39, 0
	s_cmp_ge_i32 s81, s63
	s_barrier
	s_branch .Lep_half_4

.LBB5_3:
	s_lshr_b32 s29, s35, 25
	s_add_i32 s29, s34, s29
	s_not_b32 s63, s30
	s_ashr_i32 s64, s29, 7
	s_add_i32 s65, s55, 0x18000
	v_and_b32_e32 v19, 15, v0
	v_and_b32_e32 v0, 4, v0
	s_add_u32 s30, s40, 0x80
	v_lshl_or_b32 v149, s15, 6, v19
	v_lshlrev_b32_e32 v20, 5, v1
	v_and_or_b32 v0, v18, 1, v0
	s_waitcnt vmcnt(0)
	s_barrier
	s_addc_u32 s31, s41, 0
	s_mov_b32 m0, s65
	s_nop 0
	global_load_lds_dwordx4 v148, s[30:31]
	s_add_i32 s66, s55, 0x1a000
	s_add_i32 s67, s55, 0x8000
	v_lshlrev_b32_e32 v21, 7, v149
	v_lshlrev_b32_e32 v0, 4, v0
	v_or_b32_e32 v23, 16, v20
	s_mov_b32 m0, s66
	s_nop 0
	global_load_lds_dwordx4 v152, s[30:31]
	s_add_u32 s30, s42, 0x80
	v_xor_b32_e32 v18, v0, v20
	v_bitop3_b32 v22, v21, v0, v20 bitop3:0xf6
	v_bitop3_b32 v20, v0, v20, 16 bitop3:0x1e
	v_bitop3_b32 v21, v21, v0, v23 bitop3:0xf6
	v_lshlrev_b32_e32 v0, 7, v19
	s_addc_u32 s31, s43, 0
	s_mov_b32 m0, s67
	s_nop 0
	global_load_lds_dwordx4 v146, s[30:31]
	s_add_i32 s68, s55, 0xa000
	s_add_i32 s69, s55, 0x1c000
	v_lshl_or_b32 v0, s4, 12, v0
	s_mov_b32 m0, s68
	s_nop 0
	global_load_lds_dwordx4 v150, s[30:31]
	s_add_u32 s0, s0, 0x80
	v_or3_b32 v18, v18, v0, s5
	v_or3_b32 v19, v20, v0, s5
	s_addc_u32 s1, s1, 0
	s_mov_b32 m0, s69
	s_nop 0
	global_load_lds_dwordx4 v148, s[0:1]
	v_lshlrev_b32_e32 v0, 4, v1
	s_add_i32 s70, s55, 0x1e000
	s_mov_b32 m0, s70
	s_nop 0
	global_load_lds_dwordx4 v152, s[0:1]
	v_and_b32_e32 v1, 32, v0
	v_and_b32_e32 v153, 16, v0
	v_or_b32_e32 v160, 32, v0
	v_div_scale_f32 v0, s[0:1], s13, s13, 1.0
	v_lshl_or_b32 v151, s4, 6, v1
	v_rcp_f32_e32 v1, v0
	s_cmpk_gt_i32 s34, 0x7f
	s_cselect_b64 s[30:31], -1, 0
	s_add_i32 s71, s55, 0xc000
	v_fma_f32 v20, -v0, v1, 1.0
	v_fmac_f32_e32 v1, v20, v1
	v_div_scale_f32 v20, vcc, 1.0, s13, 1.0
	v_mul_f32_e32 v23, v20, v1
	v_fma_f32 v24, -v0, v23, v20
	v_fmac_f32_e32 v23, v24, v1
	v_fma_f32 v0, -v0, v23, v20
	v_div_fmas_f32 v0, v0, v1, v23
	v_mov_b32_e32 v1, s14
	v_mul_f32_e32 v1, s13, v1
	v_div_scale_f32 v20, s[0:1], v1, v1, 1.0
	v_rcp_f32_e32 v23, v20
	s_add_i32 s72, s55, 0xe000
	s_ashr_i32 s73, s33, 31
	s_ashr_i32 s74, s2, 31
	v_fma_f32 v24, -v20, v23, 1.0
	v_fmac_f32_e32 v23, v24, v23
	v_div_scale_f32 v24, vcc, 1.0, v1, 1.0
	v_mul_f32_e32 v25, v24, v23
	v_fma_f32 v26, -v20, v25, v24
	v_fmac_f32_e32 v25, v26, v23
	v_fma_f32 v20, -v20, v25, v24
	s_waitcnt vmcnt(6)
	global_load_dword v228, v147, s[10:11]
	global_load_dword v228, v147, s[10:11]
	global_load_dword v228, v147, s[10:11]
	global_load_dword v228, v147, s[10:11]
	v_div_fmas_f32 v20, v20, v23, v25
	s_cmp_eq_u32 s64, 2
	v_div_fixup_f32 v0, v0, s13, 1.0
	v_div_fixup_f32 v161, v20, v1, 1.0
	s_cselect_b64 s[14:15], -1, 0
	s_cmpk_gt_u32 s34, 0x17f
	v_mov_b32_e32 v154, v0
	v_mov_b32_e32 v155, v0
	v_mul_f32_e32 v162, 0x40c00000, v161
	s_cselect_b64 s[34:35], -1, 0
	s_mov_b32 s36, 0x3c23d70a
	v_add_u32_e32 v163, 0, v18
	v_add_u32_e32 v164, 0, v19
	v_add_u32_e32 v165, 0, v22
	v_add_u32_e32 v166, 0, v21
	s_barrier
	s_branch .LBB5_5

.Lrs_a_5:
	s_add_u32 s82, s42, s22
	s_addc_u32 s83, s43, s23
	s_add_u32 s29, s42, 0x100
	s_addc_u32 s46, s43, 0
	s_and_b64 s[44:45], s[14:15], exec
	ds_read_b128 v[82:85], v163
	ds_read_b128 v[94:97], v163 offset:2048
	ds_read_b128 v[102:105], v164
	ds_read_b128 v[110:113], v164 offset:2048
	s_cselect_b32 s49, s39, s46
	s_cselect_b32 s48, s38, s29
	s_add_u32 s29, s40, 0x100
	s_addc_u32 s46, s41, 0
	s_and_b64 s[44:45], s[14:15], exec
	s_cselect_b32 s51, s5, s46
	s_cselect_b32 s50, s4, s29
	s_add_u32 s46, s48, 0x80
	s_addc_u32 s47, s49, 0
	s_add_u32 s44, s50, 0x80
	s_addc_u32 s45, s51, 0
	ds_read_b128 v[58:61], v165
	ds_read_b128 v[66:69], v165 offset:2048
	ds_read_b128 v[62:65], v166
	ds_read_b128 v[70:73], v166 offset:2048
	ds_read_b128 v[74:77], v165 offset:4096
	ds_read_b128 v[86:89], v165 offset:6144
	ds_read_b128 v[78:81], v166 offset:4096
	ds_read_b128 v[90:93], v166 offset:6144
	s_add_u32 s80, s82, 0x80
	s_addc_u32 s81, s83, 0
	s_mov_b32 m0, s71
	s_nop 0
	global_load_lds_dwordx4 v146, s[80:81]
	s_mov_b32 m0, s72
	s_nop 0
	global_load_lds_dwordx4 v150, s[80:81]
	s_waitcnt lgkmcnt(8)
	ds_read_b128 v[142:145], v163 offset:16384
	ds_read_b128 v[156:159], v163 offset:18432
	ds_read_b128 v[168:171], v164 offset:16384
	ds_read_b128 v[172:175], v164 offset:18432
	s_waitcnt vmcnt(12)
	s_waitcnt lgkmcnt(0)
	s_barrier
	s_waitcnt lgkmcnt(0)
	s_waitcnt vmcnt(16)
	v_mov_b32_e32 v1, v0
	v_pk_mul_f32 v[16:17], v[0:1], v[16:17]
	v_pk_mul_f32 v[14:15], v[154:155], v[14:15]
	v_pk_mul_f32 v[12:13], v[0:1], v[12:13]
	v_pk_mul_f32 v[10:11], v[154:155], v[10:11]
	v_pk_mul_f32 v[8:9], v[0:1], v[8:9]
	v_pk_mul_f32 v[6:7], v[154:155], v[6:7]
	v_pk_mul_f32 v[4:5], v[0:1], v[4:5]
	v_pk_mul_f32 v[2:3], v[154:155], v[2:3]
	s_setprio 1
	v_mfma_f32_16x16x128_f8f6f4 v[18:21], v[82:85], v[58:61], v[14:17] cbsz:4 blgp:4
	v_mfma_f32_16x16x128_f8f6f4 v[18:21], v[102:105], v[62:65], v[18:21] cbsz:4 blgp:4
	v_mfma_f32_16x16x128_f8f6f4 v[22:25], v[94:97], v[58:61], v[10:13] cbsz:4 blgp:4
	v_mfma_f32_16x16x128_f8f6f4 v[22:25], v[110:113], v[62:65], v[22:25] cbsz:4 blgp:4
	v_mfma_f32_16x16x128_f8f6f4 v[50:53], v[142:145], v[58:61], v[6:9] cbsz:4 blgp:4
	v_mfma_f32_16x16x128_f8f6f4 v[50:53], v[168:171], v[62:65], v[50:53] cbsz:4 blgp:4
	v_mfma_f32_16x16x128_f8f6f4 v[54:57], v[156:159], v[58:61], v[2:5] cbsz:4 blgp:4
	v_mfma_f32_16x16x128_f8f6f4 v[54:57], v[172:175], v[62:65], v[54:57] cbsz:4 blgp:4
	v_mfma_f32_16x16x128_f8f6f4 v[26:29], v[82:85], v[66:69], v[14:17] cbsz:4 blgp:4
	v_mfma_f32_16x16x128_f8f6f4 v[26:29], v[102:105], v[70:73], v[26:29] cbsz:4 blgp:4
	v_mfma_f32_16x16x128_f8f6f4 v[30:33], v[94:97], v[66:69], v[10:13] cbsz:4 blgp:4
	v_mfma_f32_16x16x128_f8f6f4 v[30:33], v[110:113], v[70:73], v[30:33] cbsz:4 blgp:4
	v_mfma_f32_16x16x128_f8f6f4 v[58:61], v[142:145], v[66:69], v[6:9] cbsz:4 blgp:4
	v_mfma_f32_16x16x128_f8f6f4 v[58:61], v[168:171], v[70:73], v[58:61] cbsz:4 blgp:4
	v_mfma_f32_16x16x128_f8f6f4 v[62:65], v[156:159], v[66:69], v[2:5] cbsz:4 blgp:4
	v_mfma_f32_16x16x128_f8f6f4 v[62:65], v[172:175], v[70:73], v[62:65] cbsz:4 blgp:4
	v_mfma_f32_16x16x128_f8f6f4 v[34:37], v[82:85], v[74:77], v[14:17] cbsz:4 blgp:4
	v_mfma_f32_16x16x128_f8f6f4 v[34:37], v[102:105], v[78:81], v[34:37] cbsz:4 blgp:4
	v_mfma_f32_16x16x128_f8f6f4 v[38:41], v[94:97], v[74:77], v[10:13] cbsz:4 blgp:4
	v_mfma_f32_16x16x128_f8f6f4 v[38:41], v[110:113], v[78:81], v[38:41] cbsz:4 blgp:4
	v_mfma_f32_16x16x128_f8f6f4 v[66:69], v[142:145], v[74:77], v[6:9] cbsz:4 blgp:4
	v_mfma_f32_16x16x128_f8f6f4 v[66:69], v[168:171], v[78:81], v[66:69] cbsz:4 blgp:4
	v_mfma_f32_16x16x128_f8f6f4 v[70:73], v[156:159], v[74:77], v[2:5] cbsz:4 blgp:4
	v_mfma_f32_16x16x128_f8f6f4 v[70:73], v[172:175], v[78:81], v[70:73] cbsz:4 blgp:4
	v_mfma_f32_16x16x128_f8f6f4 v[42:45], v[82:85], v[86:89], v[14:17] cbsz:4 blgp:4
	v_mfma_f32_16x16x128_f8f6f4 v[42:45], v[102:105], v[90:93], v[42:45] cbsz:4 blgp:4
	v_mfma_f32_16x16x128_f8f6f4 v[46:49], v[94:97], v[86:89], v[10:13] cbsz:4 blgp:4
	v_mfma_f32_16x16x128_f8f6f4 v[46:49], v[110:113], v[90:93], v[46:49] cbsz:4 blgp:4
	v_mfma_f32_16x16x128_f8f6f4 v[74:77], v[142:145], v[86:89], v[6:9] cbsz:4 blgp:4
	v_mfma_f32_16x16x128_f8f6f4 v[74:77], v[168:171], v[90:93], v[74:77] cbsz:4 blgp:4
	v_mfma_f32_16x16x128_f8f6f4 v[78:81], v[156:159], v[86:89], v[2:5] cbsz:4 blgp:4
	v_mfma_f32_16x16x128_f8f6f4 v[78:81], v[172:175], v[90:93], v[78:81] cbsz:4 blgp:4
	s_setprio 0
	s_barrier
	s_mov_b32 m0, s56
	s_nop 0
	global_load_lds_dwordx4 v148, s[50:51]
	s_mov_b32 m0, s57
	s_nop 0
	global_load_lds_dwordx4 v152, s[50:51]
	ds_read_b128 v[114:117], v165 offset:16384
	ds_read_b128 v[122:125], v165 offset:18432
	ds_read_b128 v[130:133], v166 offset:16384
	ds_read_b128 v[134:137], v166 offset:18432
	ds_read_b128 v[176:179], v165 offset:20480
	ds_read_b128 v[180:183], v165 offset:22528
	ds_read_b128 v[184:187], v166 offset:20480
	ds_read_b128 v[188:191], v166 offset:22528
	s_mov_b32 m0, s55
	s_nop 0
	global_load_lds_dwordx4 v146, s[48:49]
	s_mov_b32 m0, s58
	s_nop 0
	global_load_lds_dwordx4 v150, s[48:49]
	s_add_u32 s50, s50, s24
	s_addc_u32 s51, s51, s25
	s_mov_b32 m0, s59
	s_nop 0
	global_load_lds_dwordx4 v148, s[50:51]
	s_mov_b32 m0, s60
	s_nop 0
	global_load_lds_dwordx4 v152, s[50:51]
	s_waitcnt vmcnt(12)
	s_waitcnt lgkmcnt(0)
	s_barrier
	s_setprio 1
	v_mfma_f32_16x16x128_f8f6f4 v[86:89], v[82:85], v[114:117], v[14:17] cbsz:4 blgp:4
	v_mfma_f32_16x16x128_f8f6f4 v[86:89], v[102:105], v[130:133], v[86:89] cbsz:4 blgp:4
	v_mfma_f32_16x16x128_f8f6f4 v[90:93], v[94:97], v[114:117], v[10:13] cbsz:4 blgp:4
	v_mfma_f32_16x16x128_f8f6f4 v[90:93], v[110:113], v[130:133], v[90:93] cbsz:4 blgp:4
	v_mfma_f32_16x16x128_f8f6f4 v[98:101], v[82:85], v[122:125], v[14:17] cbsz:4 blgp:4
	v_mfma_f32_16x16x128_f8f6f4 v[98:101], v[102:105], v[134:137], v[98:101] cbsz:4 blgp:4
	v_mfma_f32_16x16x128_f8f6f4 v[106:109], v[94:97], v[122:125], v[10:13] cbsz:4 blgp:4
	v_mfma_f32_16x16x128_f8f6f4 v[106:109], v[110:113], v[134:137], v[106:109] cbsz:4 blgp:4
	v_mfma_f32_16x16x128_f8f6f4 v[118:121], v[82:85], v[176:179], v[14:17] cbsz:4 blgp:4
	v_mfma_f32_16x16x128_f8f6f4 v[118:121], v[102:105], v[184:187], v[118:121] cbsz:4 blgp:4
	v_mfma_f32_16x16x128_f8f6f4 v[126:129], v[94:97], v[176:179], v[10:13] cbsz:4 blgp:4
	v_mfma_f32_16x16x128_f8f6f4 v[126:129], v[110:113], v[184:187], v[126:129] cbsz:4 blgp:4
	v_mfma_f32_16x16x128_f8f6f4 v[138:141], v[82:85], v[180:183], v[14:17] cbsz:4 blgp:4
	v_mfma_f32_16x16x128_f8f6f4 v[138:141], v[102:105], v[188:191], v[138:141] cbsz:4 blgp:4
	v_mfma_f32_16x16x128_f8f6f4 v[82:85], v[94:97], v[180:183], v[10:13] cbsz:4 blgp:4
	v_mfma_f32_16x16x128_f8f6f4 v[82:85], v[110:113], v[188:191], v[82:85] cbsz:4 blgp:4
	v_mfma_f32_16x16x128_f8f6f4 v[94:97], v[142:145], v[114:117], v[6:9] cbsz:4 blgp:4
	v_mfma_f32_16x16x128_f8f6f4 v[94:97], v[168:171], v[130:133], v[94:97] cbsz:4 blgp:4
	v_mfma_f32_16x16x128_f8f6f4 v[102:105], v[156:159], v[114:117], v[2:5] cbsz:4 blgp:4
	v_mfma_f32_16x16x128_f8f6f4 v[102:105], v[172:175], v[130:133], v[102:105] cbsz:4 blgp:4
	v_mfma_f32_16x16x128_f8f6f4 v[110:113], v[142:145], v[122:125], v[6:9] cbsz:4 blgp:4
	v_mfma_f32_16x16x128_f8f6f4 v[110:113], v[168:171], v[134:137], v[110:113] cbsz:4 blgp:4
	v_mfma_f32_16x16x128_f8f6f4 v[114:117], v[156:159], v[122:125], v[2:5] cbsz:4 blgp:4
	v_mfma_f32_16x16x128_f8f6f4 v[114:117], v[172:175], v[134:137], v[114:117] cbsz:4 blgp:4
	v_mfma_f32_16x16x128_f8f6f4 v[122:125], v[142:145], v[176:179], v[6:9] cbsz:4 blgp:4
	v_mfma_f32_16x16x128_f8f6f4 v[122:125], v[168:171], v[184:187], v[122:125] cbsz:4 blgp:4
	v_mfma_f32_16x16x128_f8f6f4 v[130:133], v[156:159], v[176:179], v[2:5] cbsz:4 blgp:4
	v_mfma_f32_16x16x128_f8f6f4 v[130:133], v[172:175], v[184:187], v[130:133] cbsz:4 blgp:4
	v_mfma_f32_16x16x128_f8f6f4 v[134:137], v[142:145], v[180:183], v[6:9] cbsz:4 blgp:4
	v_mfma_f32_16x16x128_f8f6f4 v[134:137], v[168:171], v[188:191], v[134:137] cbsz:4 blgp:4
	v_mfma_f32_16x16x128_f8f6f4 v[142:145], v[156:159], v[180:183], v[2:5] cbsz:4 blgp:4
	v_mfma_f32_16x16x128_f8f6f4 v[142:145], v[172:175], v[188:191], v[142:145] cbsz:4 blgp:4
	s_setprio 0
	s_barrier
	ds_read_b128 v[156:159], v163 offset:32768
	ds_read_b128 v[168:171], v163 offset:34816
	ds_read_b128 v[172:175], v164 offset:32768
	ds_read_b128 v[176:179], v164 offset:34816
	ds_read_b128 v[180:183], v165 offset:32768
	ds_read_b128 v[184:187], v165 offset:34816
	ds_read_b128 v[188:191], v166 offset:32768
	ds_read_b128 v[192:195], v166 offset:34816
	ds_read_b128 v[196:199], v165 offset:36864
	ds_read_b128 v[200:203], v165 offset:38912
	ds_read_b128 v[204:207], v166 offset:36864
	ds_read_b128 v[208:211], v166 offset:38912
	s_add_u32 s48, s48, s22
	s_addc_u32 s49, s49, s23
	s_mov_b32 m0, s61
	s_nop 0
	global_load_lds_dwordx4 v146, s[48:49]
	s_mov_b32 m0, s62
	s_nop 0
	global_load_lds_dwordx4 v150, s[48:49]
	s_waitcnt lgkmcnt(8)
	ds_read_b128 v[212:215], v163 offset:49152
	ds_read_b128 v[216:219], v163 offset:51200
	ds_read_b128 v[220:223], v164 offset:49152
	ds_read_b128 v[224:227], v164 offset:51200
	s_waitcnt vmcnt(8)
	s_waitcnt lgkmcnt(0)
	s_barrier
	s_waitcnt lgkmcnt(0)
	s_setprio 1
	v_mfma_f32_16x16x128_f8f6f4 v[18:21], v[156:159], v[180:183], v[18:21] cbsz:4 blgp:4
	v_mfma_f32_16x16x128_f8f6f4 v[18:21], v[172:175], v[188:191], v[18:21] cbsz:4 blgp:4
	v_mfma_f32_16x16x128_f8f6f4 v[22:25], v[168:171], v[180:183], v[22:25] cbsz:4 blgp:4
	v_mfma_f32_16x16x128_f8f6f4 v[22:25], v[176:179], v[188:191], v[22:25] cbsz:4 blgp:4
	v_mfma_f32_16x16x128_f8f6f4 v[50:53], v[212:215], v[180:183], v[50:53] cbsz:4 blgp:4
	v_mfma_f32_16x16x128_f8f6f4 v[50:53], v[220:223], v[188:191], v[50:53] cbsz:4 blgp:4
	v_mfma_f32_16x16x128_f8f6f4 v[54:57], v[216:219], v[180:183], v[54:57] cbsz:4 blgp:4
	v_mfma_f32_16x16x128_f8f6f4 v[54:57], v[224:227], v[188:191], v[54:57] cbsz:4 blgp:4
	v_mfma_f32_16x16x128_f8f6f4 v[26:29], v[156:159], v[184:187], v[26:29] cbsz:4 blgp:4
	v_mfma_f32_16x16x128_f8f6f4 v[26:29], v[172:175], v[192:195], v[26:29] cbsz:4 blgp:4
	v_mfma_f32_16x16x128_f8f6f4 v[30:33], v[168:171], v[184:187], v[30:33] cbsz:4 blgp:4
	v_mfma_f32_16x16x128_f8f6f4 v[30:33], v[176:179], v[192:195], v[30:33] cbsz:4 blgp:4
	v_mfma_f32_16x16x128_f8f6f4 v[58:61], v[212:215], v[184:187], v[58:61] cbsz:4 blgp:4
	v_mfma_f32_16x16x128_f8f6f4 v[58:61], v[220:223], v[192:195], v[58:61] cbsz:4 blgp:4
	v_mfma_f32_16x16x128_f8f6f4 v[62:65], v[216:219], v[184:187], v[62:65] cbsz:4 blgp:4
	v_mfma_f32_16x16x128_f8f6f4 v[62:65], v[224:227], v[192:195], v[62:65] cbsz:4 blgp:4
	v_mfma_f32_16x16x128_f8f6f4 v[34:37], v[156:159], v[196:199], v[34:37] cbsz:4 blgp:4
	v_mfma_f32_16x16x128_f8f6f4 v[34:37], v[172:175], v[204:207], v[34:37] cbsz:4 blgp:4
	v_mfma_f32_16x16x128_f8f6f4 v[38:41], v[168:171], v[196:199], v[38:41] cbsz:4 blgp:4
	v_mfma_f32_16x16x128_f8f6f4 v[38:41], v[176:179], v[204:207], v[38:41] cbsz:4 blgp:4
	v_mfma_f32_16x16x128_f8f6f4 v[66:69], v[212:215], v[196:199], v[66:69] cbsz:4 blgp:4
	v_mfma_f32_16x16x128_f8f6f4 v[66:69], v[220:223], v[204:207], v[66:69] cbsz:4 blgp:4
	v_mfma_f32_16x16x128_f8f6f4 v[70:73], v[216:219], v[196:199], v[70:73] cbsz:4 blgp:4
	v_mfma_f32_16x16x128_f8f6f4 v[70:73], v[224:227], v[204:207], v[70:73] cbsz:4 blgp:4
	v_mfma_f32_16x16x128_f8f6f4 v[42:45], v[156:159], v[200:203], v[42:45] cbsz:4 blgp:4
	v_mfma_f32_16x16x128_f8f6f4 v[42:45], v[172:175], v[208:211], v[42:45] cbsz:4 blgp:4
	v_mfma_f32_16x16x128_f8f6f4 v[46:49], v[168:171], v[200:203], v[46:49] cbsz:4 blgp:4
	v_mfma_f32_16x16x128_f8f6f4 v[46:49], v[176:179], v[208:211], v[46:49] cbsz:4 blgp:4
	v_mfma_f32_16x16x128_f8f6f4 v[74:77], v[212:215], v[200:203], v[74:77] cbsz:4 blgp:4
	v_mfma_f32_16x16x128_f8f6f4 v[74:77], v[220:223], v[208:211], v[74:77] cbsz:4 blgp:4
	v_mfma_f32_16x16x128_f8f6f4 v[78:81], v[216:219], v[200:203], v[78:81] cbsz:4 blgp:4
	v_mfma_f32_16x16x128_f8f6f4 v[78:81], v[224:227], v[208:211], v[78:81] cbsz:4 blgp:4
	s_setprio 0
	s_barrier
	s_mov_b32 m0, s65
	s_nop 0
	global_load_lds_dwordx4 v148, s[44:45]
	s_mov_b32 m0, s66
	s_nop 0
	global_load_lds_dwordx4 v152, s[44:45]
	ds_read_b128 v[180:183], v165 offset:49152
	ds_read_b128 v[184:187], v165 offset:51200
	ds_read_b128 v[188:191], v166 offset:49152
	ds_read_b128 v[192:195], v166 offset:51200
	ds_read_b128 v[196:199], v165 offset:53248
	ds_read_b128 v[200:203], v165 offset:55296
	ds_read_b128 v[204:207], v166 offset:53248
	ds_read_b128 v[208:211], v166 offset:55296
	s_mov_b32 m0, s67
	s_nop 0
	global_load_lds_dwordx4 v146, s[46:47]
	s_mov_b32 m0, s68
	s_nop 0
	global_load_lds_dwordx4 v150, s[46:47]
	s_add_u32 s44, s44, s24
	s_addc_u32 s45, s45, s25
	s_mov_b32 m0, s69
	s_nop 0
	global_load_lds_dwordx4 v148, s[44:45]
	s_mov_b32 m0, s70
	s_nop 0
	global_load_lds_dwordx4 v152, s[44:45]
	s_waitcnt vmcnt(8)
	s_waitcnt lgkmcnt(0)
	s_barrier
	s_setprio 1
	v_mfma_f32_16x16x128_f8f6f4 v[86:89], v[156:159], v[180:183], v[86:89] cbsz:4 blgp:4
	v_mfma_f32_16x16x128_f8f6f4 v[86:89], v[172:175], v[188:191], v[86:89] cbsz:4 blgp:4
	v_mfma_f32_16x16x128_f8f6f4 v[90:93], v[168:171], v[180:183], v[90:93] cbsz:4 blgp:4
	v_mfma_f32_16x16x128_f8f6f4 v[90:93], v[176:179], v[188:191], v[90:93] cbsz:4 blgp:4
	v_mfma_f32_16x16x128_f8f6f4 v[94:97], v[212:215], v[180:183], v[94:97] cbsz:4 blgp:4
	v_mfma_f32_16x16x128_f8f6f4 v[94:97], v[220:223], v[188:191], v[94:97] cbsz:4 blgp:4
	v_mfma_f32_16x16x128_f8f6f4 v[102:105], v[216:219], v[180:183], v[102:105] cbsz:4 blgp:4
	v_mfma_f32_16x16x128_f8f6f4 v[102:105], v[224:227], v[188:191], v[102:105] cbsz:4 blgp:4
	v_mfma_f32_16x16x128_f8f6f4 v[98:101], v[156:159], v[184:187], v[98:101] cbsz:4 blgp:4
	v_mfma_f32_16x16x128_f8f6f4 v[98:101], v[172:175], v[192:195], v[98:101] cbsz:4 blgp:4
	v_mfma_f32_16x16x128_f8f6f4 v[106:109], v[168:171], v[184:187], v[106:109] cbsz:4 blgp:4
	v_mfma_f32_16x16x128_f8f6f4 v[106:109], v[176:179], v[192:195], v[106:109] cbsz:4 blgp:4
	v_mfma_f32_16x16x128_f8f6f4 v[110:113], v[212:215], v[184:187], v[110:113] cbsz:4 blgp:4
	v_mfma_f32_16x16x128_f8f6f4 v[110:113], v[220:223], v[192:195], v[110:113] cbsz:4 blgp:4
	v_mfma_f32_16x16x128_f8f6f4 v[114:117], v[216:219], v[184:187], v[114:117] cbsz:4 blgp:4
	v_mfma_f32_16x16x128_f8f6f4 v[114:117], v[224:227], v[192:195], v[114:117] cbsz:4 blgp:4
	v_mfma_f32_16x16x128_f8f6f4 v[118:121], v[156:159], v[196:199], v[118:121] cbsz:4 blgp:4
	v_mfma_f32_16x16x128_f8f6f4 v[118:121], v[172:175], v[204:207], v[118:121] cbsz:4 blgp:4
	v_mfma_f32_16x16x128_f8f6f4 v[126:129], v[168:171], v[196:199], v[126:129] cbsz:4 blgp:4
	v_mfma_f32_16x16x128_f8f6f4 v[126:129], v[176:179], v[204:207], v[126:129] cbsz:4 blgp:4
	v_mfma_f32_16x16x128_f8f6f4 v[122:125], v[212:215], v[196:199], v[122:125] cbsz:4 blgp:4
	v_mfma_f32_16x16x128_f8f6f4 v[122:125], v[220:223], v[204:207], v[122:125] cbsz:4 blgp:4
	v_mfma_f32_16x16x128_f8f6f4 v[130:133], v[216:219], v[196:199], v[130:133] cbsz:4 blgp:4
	v_mfma_f32_16x16x128_f8f6f4 v[130:133], v[224:227], v[204:207], v[130:133] cbsz:4 blgp:4
	v_mfma_f32_16x16x128_f8f6f4 v[138:141], v[156:159], v[200:203], v[138:141] cbsz:4 blgp:4
	v_mfma_f32_16x16x128_f8f6f4 v[138:141], v[172:175], v[208:211], v[138:141] cbsz:4 blgp:4
	v_mfma_f32_16x16x128_f8f6f4 v[82:85], v[168:171], v[200:203], v[82:85] cbsz:4 blgp:4
	v_mfma_f32_16x16x128_f8f6f4 v[82:85], v[176:179], v[208:211], v[82:85] cbsz:4 blgp:4
	v_mfma_f32_16x16x128_f8f6f4 v[134:137], v[212:215], v[200:203], v[134:137] cbsz:4 blgp:4
	v_mfma_f32_16x16x128_f8f6f4 v[134:137], v[220:223], v[208:211], v[134:137] cbsz:4 blgp:4
	v_mfma_f32_16x16x128_f8f6f4 v[142:145], v[216:219], v[200:203], v[142:145] cbsz:4 blgp:4
	v_mfma_f32_16x16x128_f8f6f4 v[142:145], v[224:227], v[208:211], v[142:145] cbsz:4 blgp:4
	s_setprio 0
	s_andn2_b64 vcc, exec, s[34:35]
	s_barrier
	s_cbranch_vccnz .LBB5_4
	s_ashr_i32 s29, s28, 31
	s_lshl_b64 s[44:45], s[28:29], 10
	s_add_u32 s44, s10, s44
	s_addc_u32 s45, s11, s45
	s_add_u32 s29, s42, 0x200
	s_addc_u32 s79, s43, 0
	s_add_u32 s80, s40, 0x200
	s_addc_u32 s81, s41, 0
	s_add_u32 s40, s82, 0x180
	s_addc_u32 s41, s83, 0
	s_mov_b32 s82, 4
	s_cmp_eq_u32 s64, s82
	s_cselect_b64 s[42:43], -1, 0
	s_cmp_lg_u32 s64, s82
	s_cbranch_scc1 .LBB5_15

.Lfunc_end5:
	.size	_Z6k_gemmI4Epi8ILi1ELb1ELb1EEEv4GemmT_iiii, .Lfunc_end5-_Z6k_gemmI4Epi8ILi1ELb1ELb1EEEv4GemmT_iiii
	.set _Z6k_gemmI4Epi8ILi1ELb1ELb1EEEv4GemmT_iiii.num_vgpr, 232
	.set _Z6k_gemmI4Epi8ILi1ELb1ELb1EEEv4GemmT_iiii.num_agpr, 0
	.set _Z6k_gemmI4Epi8ILi1ELb1ELb1EEEv4GemmT_iiii.numbered_sgpr, 84
	.set _Z6k_gemmI4Epi8ILi1ELb1ELb1EEEv4GemmT_iiii.num_named_barrier, 0
	.set _Z6k_gemmI4Epi8ILi1ELb1ELb1EEEv4GemmT_iiii.private_seg_size, 0
	.set _Z6k_gemmI4Epi8ILi1ELb1ELb1EEEv4GemmT_iiii.uses_vcc, 1
	.set _Z6k_gemmI4Epi8ILi1ELb1ELb1EEEv4GemmT_iiii.uses_flat_scratch, 0
	.set _Z6k_gemmI4Epi8ILi1ELb1ELb1EEEv4GemmT_iiii.has_dyn_sized_stack, 0
	.set _Z6k_gemmI4Epi8ILi1ELb1ELb1EEEv4GemmT_iiii.has_recursion, 0
	.set _Z6k_gemmI4Epi8ILi1ELb1ELb1EEEv4GemmT_iiii.has_indirect_call, 0

amdhsa.kernels:
  - .agpr_count:     0
    .args:
      - .offset:         0
        .size:           80
        .value_kind:     by_value
    .group_segment_fixed_size: 8192
    .kernarg_segment_align: 8
    .kernarg_segment_size: 80
    .language:       OpenCL C
    .language_version:
      - 2
      - 0
    .max_flat_workgroup_size: 256
    .name:           _Z6k_prep8PrepArgs
    .private_segment_fixed_size: 0
    .sgpr_count:     35
    .sgpr_spill_count: 0
    .symbol:         _Z6k_prep8PrepArgs.kd
    .uniform_work_group_size: 1
    .uses_dynamic_stack: false
    .vgpr_count:     45
    .vgpr_spill_count: 0
    .wavefront_size: 64
  - .agpr_count:     4
    .args:
      - .actual_access:  read_only
        .address_space:  global
        .offset:         0
        .size:           8
        .value_kind:     global_buffer
      - .actual_access:  read_only
        .address_space:  global
        .offset:         8
        .size:           8
        .value_kind:     global_buffer
      - .actual_access:  read_only
        .address_space:  global
        .offset:         16
        .size:           8
        .value_kind:     global_buffer
      - .actual_access:  write_only
        .address_space:  global
        .offset:         24
        .size:           8
        .value_kind:     global_buffer
      - .actual_access:  write_only
        .address_space:  global
        .offset:         32
        .size:           8
        .value_kind:     global_buffer
    .group_segment_fixed_size: 36096
    .kernarg_segment_align: 8
    .kernarg_segment_size: 40
    .language:       OpenCL C
    .language_version:
      - 2
      - 0
    .max_flat_workgroup_size: 256
    .name:           _Z7k_gatesPKfPKtS0_PhPf
    .private_segment_fixed_size: 0
    .sgpr_count:     18
    .sgpr_spill_count: 0
    .symbol:         _Z7k_gatesPKfPKtS0_PhPf.kd
    .uniform_work_group_size: 1
    .uses_dynamic_stack: false
    .vgpr_count:     124
    .vgpr_spill_count: 0
    .wavefront_size: 64
  - .agpr_count:     0
    .args:
      - .actual_access:  read_only
        .address_space:  global
        .offset:         0
        .size:           8
        .value_kind:     global_buffer
      - .actual_access:  read_only
        .address_space:  global
        .offset:         8
        .size:           8
        .value_kind:     global_buffer
      - .actual_access:  write_only
        .address_space:  global
        .offset:         16
        .size:           8
        .value_kind:     global_buffer
      - .offset:         24
        .size:           4
        .value_kind:     by_value
    .group_segment_fixed_size: 0
    .kernarg_segment_align: 8
    .kernarg_segment_size: 28
    .language:       OpenCL C
    .language_version:
      - 2
      - 0
    .max_flat_workgroup_size: 256
    .name:           _Z5k_mixPKhPKfPhi
    .private_segment_fixed_size: 0
    .sgpr_count:     40
    .sgpr_spill_count: 0
    .symbol:         _Z5k_mixPKhPKfPhi.kd
    .uniform_work_group_size: 1
    .uses_dynamic_stack: false
    .vgpr_count:     124
    .vgpr_spill_count: 0
    .wavefront_size: 64
  - .agpr_count:     0
    .args:
      - .actual_access:  read_only
        .address_space:  global
        .offset:         0
        .size:           8
        .value_kind:     global_buffer
      - .actual_access:  read_only
        .address_space:  global
        .offset:         8
        .size:           8
        .value_kind:     global_buffer
      - .actual_access:  write_only
        .address_space:  global
        .offset:         16
        .size:           8
        .value_kind:     global_buffer
    .group_segment_fixed_size: 0
    .kernarg_segment_align: 8
    .kernarg_segment_size: 24
    .language:       OpenCL C
    .language_version:
      - 2
      - 0
    .max_flat_workgroup_size: 256
    .name:           _Z7k_finalPKfS0_Pf
    .private_segment_fixed_size: 0
    .sgpr_count:     16
    .sgpr_spill_count: 0
    .symbol:         _Z7k_finalPKfS0_Pf.kd
    .uniform_work_group_size: 1
    .uses_dynamic_stack: false
    .vgpr_count:     16
    .vgpr_spill_count: 0
    .wavefront_size: 64
  - .agpr_count:     0
    .args:
      - .offset:         0
        .size:           24
        .value_kind:     by_value
      - .offset:         24
        .size:           32
        .value_kind:     by_value
      - .offset:         56
        .size:           4
        .value_kind:     by_value
      - .offset:         60
        .size:           4
        .value_kind:     by_value
      - .offset:         64
        .size:           4
        .value_kind:     by_value
      - .offset:         68
        .size:           4
        .value_kind:     by_value
      - .offset:         72
        .size:           4
        .value_kind:     hidden_block_count_x
      - .offset:         76
        .size:           4
        .value_kind:     hidden_block_count_y
      - .offset:         80
        .size:           4
        .value_kind:     hidden_block_count_z
      - .offset:         84
        .size:           2
        .value_kind:     hidden_group_size_x
      - .offset:         86
        .size:           2
        .value_kind:     hidden_group_size_y
      - .offset:         88
        .size:           2
        .value_kind:     hidden_group_size_z
      - .offset:         90
        .size:           2
        .value_kind:     hidden_remainder_x
      - .offset:         92
        .size:           2
        .value_kind:     hidden_remainder_y
      - .offset:         94
        .size:           2
        .value_kind:     hidden_remainder_z
      - .offset:         112
        .size:           8
        .value_kind:     hidden_global_offset_x
      - .offset:         120
        .size:           8
        .value_kind:     hidden_global_offset_y
      - .offset:         128
        .size:           8
        .value_kind:     hidden_global_offset_z
      - .offset:         136
        .size:           2
        .value_kind:     hidden_grid_dims
      - .offset:         192
        .size:           4
        .value_kind:     hidden_dynamic_lds_size
    .group_segment_fixed_size: 0
    .kernarg_segment_align: 8
    .kernarg_segment_size: 328
    .language:       OpenCL C
    .language_version:
      - 2
      - 0
    .max_flat_workgroup_size: 512
    .name:           _Z6k_gemmI4Epi8ILi0ELb1ELb1EEEv4GemmT_iiii
    .private_segment_fixed_size: 0
    .sgpr_count:     92
    .sgpr_spill_count: 0
    .symbol:         _Z6k_gemmI4Epi8ILi0ELb1ELb1EEEv4GemmT_iiii.kd
    .uniform_work_group_size: 1
    .uses_dynamic_stack: false
    .vgpr_count:     248
    .vgpr_spill_count: 0
    .wavefront_size: 64
  - .agpr_count:     0
    .args:
      - .offset:         0
        .size:           24
        .value_kind:     by_value
      - .offset:         24
        .size:           32
        .value_kind:     by_value
      - .offset:         56
        .size:           4
        .value_kind:     by_value
      - .offset:         60
        .size:           4
        .value_kind:     by_value
      - .offset:         64
        .size:           4
        .value_kind:     by_value
      - .offset:         68
        .size:           4
        .value_kind:     by_value
      - .offset:         72
        .size:           4
        .value_kind:     hidden_block_count_x
      - .offset:         76
        .size:           4
        .value_kind:     hidden_block_count_y
      - .offset:         80
        .size:           4
        .value_kind:     hidden_block_count_z
      - .offset:         84
        .size:           2
        .value_kind:     hidden_group_size_x
      - .offset:         86
        .size:           2
        .value_kind:     hidden_group_size_y
      - .offset:         88
        .size:           2
        .value_kind:     hidden_group_size_z
      - .offset:         90
        .size:           2
        .value_kind:     hidden_remainder_x
      - .offset:         92
        .size:           2
        .value_kind:     hidden_remainder_y
      - .offset:         94
        .size:           2
        .value_kind:     hidden_remainder_z
      - .offset:         112
        .size:           8
        .value_kind:     hidden_global_offset_x
      - .offset:         120
        .size:           8
        .value_kind:     hidden_global_offset_y
      - .offset:         128
        .size:           8
        .value_kind:     hidden_global_offset_z
      - .offset:         136
        .size:           2
        .value_kind:     hidden_grid_dims
      - .offset:         192
        .size:           4
        .value_kind:     hidden_dynamic_lds_size
    .group_segment_fixed_size: 0
    .kernarg_segment_align: 8
    .kernarg_segment_size: 328
    .language:       OpenCL C
    .language_version:
      - 2
      - 0
    .max_flat_workgroup_size: 512
    .name:           _Z6k_gemmI4Epi8ILi1ELb1ELb1EEEv4GemmT_iiii
    .private_segment_fixed_size: 0
    .sgpr_count:     90
    .sgpr_spill_count: 0
    .symbol:         _Z6k_gemmI4Epi8ILi1ELb1ELb1EEEv4GemmT_iiii.kd
    .uniform_work_group_size: 1
    .uses_dynamic_stack: false
    .vgpr_count:     232
    .vgpr_spill_count: 0
    .wavefront_size: 64
  - .agpr_count:     0
    .args:
      - .offset:         0
        .size:           24
        .value_kind:     by_value
      - .offset:         24
        .size:           32
        .value_kind:     by_value
      - .offset:         56
        .size:           4
        .value_kind:     by_value
      - .offset:         60
        .size:           4
        .value_kind:     by_value
      - .offset:         64
        .size:           4
        .value_kind:     by_value
      - .offset:         68
        .size:           4
        .value_kind:     by_value
      - .offset:         72
        .size:           4
        .value_kind:     hidden_block_count_x
      - .offset:         76
        .size:           4
        .value_kind:     hidden_block_count_y
      - .offset:         80
        .size:           4
        .value_kind:     hidden_block_count_z
      - .offset:         84
        .size:           2
        .value_kind:     hidden_group_size_x
      - .offset:         86
        .size:           2
        .value_kind:     hidden_group_size_y
      - .offset:         88
        .size:           2
        .value_kind:     hidden_group_size_z
      - .offset:         90
        .size:           2
        .value_kind:     hidden_remainder_x
      - .offset:         92
        .size:           2
        .value_kind:     hidden_remainder_y
      - .offset:         94
        .size:           2
        .value_kind:     hidden_remainder_z
      - .offset:         112
        .size:           8
        .value_kind:     hidden_global_offset_x
      - .offset:         120
        .size:           8
        .value_kind:     hidden_global_offset_y
      - .offset:         128
        .size:           8
        .value_kind:     hidden_global_offset_z
      - .offset:         136
        .size:           2
        .value_kind:     hidden_grid_dims
      - .offset:         192
        .size:           4
        .value_kind:     hidden_dynamic_lds_size
    .group_segment_fixed_size: 0
    .kernarg_segment_align: 8
    .kernarg_segment_size: 328
    .language:       OpenCL C
    .language_version:
      - 2
      - 0
    .max_flat_workgroup_size: 512
    .name:           _Z6k_gemmI8EpiTowerEv4GemmT_iiii
    .private_segment_fixed_size: 0
    .sgpr_count:     92
    .sgpr_spill_count: 0
    .symbol:         _Z6k_gemmI8EpiTowerEv4GemmT_iiii.kd
    .uniform_work_group_size: 1
    .uses_dynamic_stack: false
    .vgpr_count:     230
    .vgpr_spill_count: 0
    .wavefront_size: 64
